# speedup vs baseline: 1.1017x; 1.0089x over previous
.LBB1_41:
	s_add_i32 s2, 0, 0x10200
	v_mov_b32_e32 v2, s2
	ds_read_b128 v[2:5], v2
	v_lshl_add_u32 v6, v8, 2, s4
	ds_read_b32 v56, v6 offset:256
	s_waitcnt lgkmcnt(0)
	v_lshrrev_b32_e32 v5, 5, v1
	v_lshlrev_b32_e32 v98, 4, v5
	v_add_u32_e32 v3, 0, v98
	v_add_u32_e32 v99, 0x10000, v3
	ds_read_b128 v[6:9], v99
	ds_read_b128 v[10:13], v99 offset:256
	v_mov_b32_e32 v19, s4
	ds_read_b128 v[14:17], v99 offset:32
	ds_read_b128 v[20:23], v99 offset:288
	s_add_i32 s2, 0, 0x10210
	v_mov_b32_e32 v57, s2
	s_waitcnt lgkmcnt(0)
	v_pk_fma_f32 v[44:45], v[18:19], v[6:7], v[10:11] op_sel_hi:[0,1,1]
	v_pk_fma_f32 v[46:47], v[18:19], v[8:9], v[12:13] op_sel_hi:[0,1,1]
	ds_read_b128 v[6:9], v99 offset:320
	ds_read_b128 v[10:13], v99 offset:64
	ds_read_b128 v[24:27], v99 offset:96
	ds_read_b128 v[28:31], v99 offset:352
	v_pk_fma_f32 v[40:41], v[18:19], v[14:15], v[20:21] op_sel_hi:[0,1,1]
	v_pk_fma_f32 v[42:43], v[18:19], v[16:17], v[22:23] op_sel_hi:[0,1,1]
	s_waitcnt lgkmcnt(0)
	v_pk_fma_f32 v[36:37], v[18:19], v[10:11], v[6:7] op_sel_hi:[0,1,1]
	v_pk_fma_f32 v[38:39], v[18:19], v[12:13], v[8:9] op_sel_hi:[0,1,1]
	v_pk_fma_f32 v[32:33], v[18:19], v[24:25], v[28:29] op_sel_hi:[0,1,1]
	v_pk_fma_f32 v[34:35], v[18:19], v[26:27], v[30:31] op_sel_hi:[0,1,1]
	ds_read_b128 v[6:9], v99 offset:384
	ds_read_b128 v[10:13], v99 offset:128
	ds_read_b128 v[14:17], v99 offset:160
	ds_read_b128 v[48:51], v99 offset:416
	ds_read_b128 v[20:23], v99 offset:192
	ds_read_b128 v[24:27], v99 offset:448
	s_waitcnt lgkmcnt(0)
	v_pk_fma_f32 v[28:29], v[18:19], v[10:11], v[6:7] op_sel_hi:[0,1,1]
	v_pk_fma_f32 v[30:31], v[18:19], v[12:13], v[8:9] op_sel_hi:[0,1,1]
	ds_read_b128 v[10:13], v99 offset:224
	ds_read_b128 v[52:55], v99 offset:480
	ds_read_b128 v[6:9], v57
	s_waitcnt lgkmcnt(0)
	v_lshl_add_u32 v7, v1, 2, s4
	v_fmac_f32_e32 v4, v18, v2
	v_pk_fma_f32 v[2:3], v[18:19], v[20:21], v[24:25] op_sel_hi:[0,1,1]
	v_pk_fma_f32 v[20:21], v[18:19], v[22:23], v[26:27] op_sel_hi:[0,1,1]
	ds_read_b32 v7, v7
	v_pk_fma_f32 v[22:23], v[18:19], v[10:11], v[52:53] op_sel_hi:[0,1,1]
	v_mbcnt_lo_u32_b32 v11, -1, 0
	v_mbcnt_hi_u32_b32 v52, -1, v11
	v_and_b32_e32 v11, 64, v52
	v_add_u32_e32 v53, 64, v11
	v_xor_b32_e32 v11, 1, v52
	v_cmp_lt_i32_e32 vcc, v11, v53
	v_max_f32_e32 v10, v56, v56
	s_waitcnt lgkmcnt(0)
	v_max_f32_e32 v7, v7, v7
	v_cndmask_b32_e32 v11, v52, v11, vcc
	v_max_f32_e32 v24, v7, v10
	v_lshlrev_b32_e32 v11, 2, v11
	s_add_i32 s2, 0, 0x10220
	ds_bpermute_b32 v25, v11, v24
	v_min_f32_e32 v7, v7, v10
	v_mov_b32_e32 v9, s2
	v_pk_fma_f32 v[26:27], v[18:19], v[12:13], v[54:55] op_sel_hi:[0,1,1]
	ds_bpermute_b32 v54, v11, v7
	ds_read_b128 v[10:13], v9
	s_waitcnt lgkmcnt(0)
	v_xor_b32_e32 v11, 2, v52
	v_cmp_lt_i32_e32 vcc, v11, v53
	v_fmac_f32_e32 v8, v18, v6
	v_max_f32_e32 v6, v25, v25
	v_cndmask_b32_e32 v11, v52, v11, vcc
	v_max_f32_e32 v6, v24, v6
	v_max_f32_e32 v9, v54, v54
	v_lshlrev_b32_e32 v11, 2, v11
	ds_bpermute_b32 v13, v11, v6
	v_min_f32_e32 v7, v7, v9
	ds_bpermute_b32 v9, v11, v7
	v_fmac_f32_e32 v12, v18, v10
	s_add_i32 s2, 0, 0x10230
	s_waitcnt lgkmcnt(0)
	v_max_f32_e32 v13, v13, v13
	v_max_f32_e32 v13, v6, v13
	v_max_f32_e32 v6, v9, v9
	v_xor_b32_e32 v9, 4, v52
	v_cmp_lt_i32_e32 vcc, v9, v53
	v_min_f32_e32 v55, v7, v6
	v_pk_fma_f32 v[6:7], v[18:19], v[14:15], v[48:49] op_sel_hi:[0,1,1]
	v_cndmask_b32_e32 v9, v52, v9, vcc
	v_lshlrev_b32_e32 v9, 2, v9
	ds_bpermute_b32 v54, v9, v13
	ds_bpermute_b32 v9, v9, v55
	v_mov_b32_e32 v11, s2
	s_movk_i32 s2, 0xc0
	v_pk_fma_f32 v[24:25], v[18:19], v[16:17], v[50:51] op_sel_hi:[0,1,1]
	s_waitcnt lgkmcnt(0)
	v_max_f32_e32 v14, v54, v54
	v_max_f32_e32 v13, v13, v14
	v_xor_b32_e32 v14, 8, v52
	v_cmp_lt_i32_e32 vcc, v14, v53
	v_max_f32_e32 v9, v9, v9
	v_min_f32_e32 v9, v55, v9
	v_cndmask_b32_e32 v14, v52, v14, vcc
	v_lshlrev_b32_e32 v14, 2, v14
	ds_bpermute_b32 v48, v14, v13
	ds_bpermute_b32 v49, v14, v9
	ds_read_b128 v[14:17], v11
	v_mad_u32_u24 v125, v5, s2, v19
	ds_read_b128 v[58:61], v125
	s_waitcnt lgkmcnt(0)
	v_max_f32_e32 v10, v48, v48
	v_max_f32_e32 v10, v13, v10
	v_xor_b32_e32 v13, 16, v52
	v_cmp_lt_i32_e32 vcc, v13, v53
	v_max_f32_e32 v11, v49, v49
	v_min_f32_e32 v9, v9, v11
	v_cndmask_b32_e32 v13, v52, v13, vcc
	v_lshlrev_b32_e32 v13, 2, v13
	ds_bpermute_b32 v15, v13, v10
	ds_bpermute_b32 v11, v13, v9
	v_fmac_f32_e32 v16, v18, v14
	ds_read_b128 v[86:89], v125 offset:16
	ds_read_b128 v[132:135], v125 offset:32
	s_waitcnt lgkmcnt(0)
	v_max_f32_e32 v13, v15, v15
	v_max_f32_e32 v10, v10, v13
	v_xor_b32_e32 v13, 32, v52
	v_cmp_lt_i32_e32 vcc, v13, v53
	v_max_f32_e32 v11, v11, v11
	v_min_f32_e32 v9, v9, v11
	v_cndmask_b32_e32 v13, v52, v13, vcc
	v_lshlrev_b32_e32 v13, 2, v13
	ds_bpermute_b32 v15, v13, v10
	ds_bpermute_b32 v11, v13, v9
	ds_read_b128 v[136:139], v125 offset:48
	ds_read_b128 v[148:151], v125 offset:64
	ds_read_b128 v[158:161], v125 offset:80
	ds_read_b128 v[180:183], v125 offset:96
	s_waitcnt lgkmcnt(0)
	v_max_f32_e32 v13, v15, v15
	v_max_f32_e32 v11, v11, v11
	v_max_f32_e32 v10, v10, v13
	v_min_f32_e32 v9, v9, v11
	v_mul_f32_e32 v11, v10, v4
	v_mul_f32_e32 v13, v9, v4
	v_max_f32_e32 v131, v11, v13
	v_mul_f32_e32 v11, v10, v8
	v_mul_f32_e32 v13, v9, v8
	v_max_f32_e32 v130, v11, v13
	v_mul_f32_e32 v11, v10, v12
	v_mul_f32_e32 v13, v9, v12
	v_mul_f32_e32 v10, v10, v16
	v_mul_f32_e32 v9, v9, v16
	v_max_f32_e32 v128, v10, v9
	v_max_f32_e32 v129, v11, v13
	s_waitcnt lgkmcnt(0)
	ds_read_b128 v[68:71], v125 offset:112
	ds_read_b128 v[92:95], v125 offset:128
	ds_read_b128 v[100:103], v125 offset:144
	ds_read_b128 v[104:107], v125 offset:160
	ds_read_b128 v[108:111], v125 offset:176
	v_mov_b32_e32 v140, v4
	v_mov_b32_e32 v141, v8
	v_mov_b32_e32 v142, v12
	v_mov_b32_e32 v143, v16
	v_mov_b32_e32 v144, v131
	v_mov_b32_e32 v145, v130
	v_mov_b32_e32 v146, v129
	v_mov_b32_e32 v147, v128
	v_mov_b32_e32 v152, 0
	v_mov_b32_e32 v153, 0
	v_mov_b32_e32 v154, 0
	v_mov_b32_e32 v155, 0
	v_mov_b32_e32 v164, 0
	v_mov_b32_e32 v165, 0
	v_mov_b32_e32 v166, 0
	v_mov_b32_e32 v167, 0
	v_pk_fma_f32 v[112:113], v[58:59], v[140:141], v[144:145] op_sel:[0,0,0] op_sel_hi:[0,1,1] neg_lo:[0,0,1] neg_hi:[0,0,1]
	v_pk_fma_f32 v[114:115], v[58:59], v[142:143], v[146:147] op_sel:[0,0,0] op_sel_hi:[0,1,1] neg_lo:[0,0,1] neg_hi:[0,0,1]
	v_exp_f32_e32 v112, v112
	v_exp_f32_e32 v113, v113
	v_exp_f32_e32 v114, v114
	v_exp_f32_e32 v115, v115
	v_pk_fma_f32 v[116:117], v[58:59], v[140:141], v[144:145] op_sel:[1,0,0] op_sel_hi:[1,1,1] neg_lo:[0,0,1] neg_hi:[0,0,1]
	v_pk_fma_f32 v[118:119], v[58:59], v[142:143], v[146:147] op_sel:[1,0,0] op_sel_hi:[1,1,1] neg_lo:[0,0,1] neg_hi:[0,0,1]
	v_exp_f32_e32 v116, v116
	v_exp_f32_e32 v117, v117
	v_exp_f32_e32 v118, v118
	v_exp_f32_e32 v119, v119
	v_pk_add_f32 v[152:153], v[152:153], v[112:113]
	v_pk_add_f32 v[154:155], v[154:155], v[114:115]
	v_pk_fma_f32 v[164:165], v[112:113], v[58:59], v[164:165] op_sel:[0,0,0] op_sel_hi:[1,0,1]
	v_pk_fma_f32 v[166:167], v[114:115], v[58:59], v[166:167] op_sel:[0,0,0] op_sel_hi:[1,0,1]
	v_pk_add_f32 v[152:153], v[152:153], v[116:117]
	v_pk_add_f32 v[154:155], v[154:155], v[118:119]
	v_pk_fma_f32 v[164:165], v[116:117], v[58:59], v[164:165] op_sel:[0,1,0] op_sel_hi:[1,1,1]
	v_pk_fma_f32 v[166:167], v[118:119], v[58:59], v[166:167] op_sel:[0,1,0] op_sel_hi:[1,1,1]
	v_pk_fma_f32 v[112:113], v[60:61], v[140:141], v[144:145] op_sel:[0,0,0] op_sel_hi:[0,1,1] neg_lo:[0,0,1] neg_hi:[0,0,1]
	v_pk_fma_f32 v[114:115], v[60:61], v[142:143], v[146:147] op_sel:[0,0,0] op_sel_hi:[0,1,1] neg_lo:[0,0,1] neg_hi:[0,0,1]
	v_exp_f32_e32 v112, v112
	v_exp_f32_e32 v113, v113
	v_exp_f32_e32 v114, v114
	v_exp_f32_e32 v115, v115
	v_pk_fma_f32 v[116:117], v[60:61], v[140:141], v[144:145] op_sel:[1,0,0] op_sel_hi:[1,1,1] neg_lo:[0,0,1] neg_hi:[0,0,1]
	v_pk_fma_f32 v[118:119], v[60:61], v[142:143], v[146:147] op_sel:[1,0,0] op_sel_hi:[1,1,1] neg_lo:[0,0,1] neg_hi:[0,0,1]
	v_exp_f32_e32 v116, v116
	v_exp_f32_e32 v117, v117
	v_exp_f32_e32 v118, v118
	v_exp_f32_e32 v119, v119
	v_pk_add_f32 v[152:153], v[152:153], v[112:113]
	v_pk_add_f32 v[154:155], v[154:155], v[114:115]
	v_pk_fma_f32 v[164:165], v[112:113], v[60:61], v[164:165] op_sel:[0,0,0] op_sel_hi:[1,0,1]
	v_pk_fma_f32 v[166:167], v[114:115], v[60:61], v[166:167] op_sel:[0,0,0] op_sel_hi:[1,0,1]
	v_pk_add_f32 v[152:153], v[152:153], v[116:117]
	v_pk_add_f32 v[154:155], v[154:155], v[118:119]
	v_pk_fma_f32 v[164:165], v[116:117], v[60:61], v[164:165] op_sel:[0,1,0] op_sel_hi:[1,1,1]
	v_pk_fma_f32 v[166:167], v[118:119], v[60:61], v[166:167] op_sel:[0,1,0] op_sel_hi:[1,1,1]
	v_pk_fma_f32 v[112:113], v[86:87], v[140:141], v[144:145] op_sel:[0,0,0] op_sel_hi:[0,1,1] neg_lo:[0,0,1] neg_hi:[0,0,1]
	v_pk_fma_f32 v[114:115], v[86:87], v[142:143], v[146:147] op_sel:[0,0,0] op_sel_hi:[0,1,1] neg_lo:[0,0,1] neg_hi:[0,0,1]
	v_exp_f32_e32 v112, v112
	v_exp_f32_e32 v113, v113
	v_exp_f32_e32 v114, v114
	v_exp_f32_e32 v115, v115
	v_pk_fma_f32 v[116:117], v[86:87], v[140:141], v[144:145] op_sel:[1,0,0] op_sel_hi:[1,1,1] neg_lo:[0,0,1] neg_hi:[0,0,1]
	v_pk_fma_f32 v[118:119], v[86:87], v[142:143], v[146:147] op_sel:[1,0,0] op_sel_hi:[1,1,1] neg_lo:[0,0,1] neg_hi:[0,0,1]
	v_exp_f32_e32 v116, v116
	v_exp_f32_e32 v117, v117
	v_exp_f32_e32 v118, v118
	v_exp_f32_e32 v119, v119
	v_pk_add_f32 v[152:153], v[152:153], v[112:113]
	v_pk_add_f32 v[154:155], v[154:155], v[114:115]
	v_pk_fma_f32 v[164:165], v[112:113], v[86:87], v[164:165] op_sel:[0,0,0] op_sel_hi:[1,0,1]
	v_pk_fma_f32 v[166:167], v[114:115], v[86:87], v[166:167] op_sel:[0,0,0] op_sel_hi:[1,0,1]
	v_pk_add_f32 v[152:153], v[152:153], v[116:117]
	v_pk_add_f32 v[154:155], v[154:155], v[118:119]
	v_pk_fma_f32 v[164:165], v[116:117], v[86:87], v[164:165] op_sel:[0,1,0] op_sel_hi:[1,1,1]
	v_pk_fma_f32 v[166:167], v[118:119], v[86:87], v[166:167] op_sel:[0,1,0] op_sel_hi:[1,1,1]
	v_pk_fma_f32 v[112:113], v[88:89], v[140:141], v[144:145] op_sel:[0,0,0] op_sel_hi:[0,1,1] neg_lo:[0,0,1] neg_hi:[0,0,1]
	v_pk_fma_f32 v[114:115], v[88:89], v[142:143], v[146:147] op_sel:[0,0,0] op_sel_hi:[0,1,1] neg_lo:[0,0,1] neg_hi:[0,0,1]
	v_exp_f32_e32 v112, v112
	v_exp_f32_e32 v113, v113
	v_exp_f32_e32 v114, v114
	v_exp_f32_e32 v115, v115
	v_pk_fma_f32 v[116:117], v[88:89], v[140:141], v[144:145] op_sel:[1,0,0] op_sel_hi:[1,1,1] neg_lo:[0,0,1] neg_hi:[0,0,1]
	v_pk_fma_f32 v[118:119], v[88:89], v[142:143], v[146:147] op_sel:[1,0,0] op_sel_hi:[1,1,1] neg_lo:[0,0,1] neg_hi:[0,0,1]
	v_exp_f32_e32 v116, v116
	v_exp_f32_e32 v117, v117
	v_exp_f32_e32 v118, v118
	v_exp_f32_e32 v119, v119
	v_pk_add_f32 v[152:153], v[152:153], v[112:113]
	v_pk_add_f32 v[154:155], v[154:155], v[114:115]
	v_pk_fma_f32 v[164:165], v[112:113], v[88:89], v[164:165] op_sel:[0,0,0] op_sel_hi:[1,0,1]
	v_pk_fma_f32 v[166:167], v[114:115], v[88:89], v[166:167] op_sel:[0,0,0] op_sel_hi:[1,0,1]
	v_pk_add_f32 v[152:153], v[152:153], v[116:117]
	v_pk_add_f32 v[154:155], v[154:155], v[118:119]
	v_pk_fma_f32 v[164:165], v[116:117], v[88:89], v[164:165] op_sel:[0,1,0] op_sel_hi:[1,1,1]
	v_pk_fma_f32 v[166:167], v[118:119], v[88:89], v[166:167] op_sel:[0,1,0] op_sel_hi:[1,1,1]
	v_pk_fma_f32 v[112:113], v[132:133], v[140:141], v[144:145] op_sel:[0,0,0] op_sel_hi:[0,1,1] neg_lo:[0,0,1] neg_hi:[0,0,1]
	v_pk_fma_f32 v[114:115], v[132:133], v[142:143], v[146:147] op_sel:[0,0,0] op_sel_hi:[0,1,1] neg_lo:[0,0,1] neg_hi:[0,0,1]
	v_exp_f32_e32 v112, v112
	v_exp_f32_e32 v113, v113
	v_exp_f32_e32 v114, v114
	v_exp_f32_e32 v115, v115
	v_pk_fma_f32 v[116:117], v[132:133], v[140:141], v[144:145] op_sel:[1,0,0] op_sel_hi:[1,1,1] neg_lo:[0,0,1] neg_hi:[0,0,1]
	v_pk_fma_f32 v[118:119], v[132:133], v[142:143], v[146:147] op_sel:[1,0,0] op_sel_hi:[1,1,1] neg_lo:[0,0,1] neg_hi:[0,0,1]
	v_exp_f32_e32 v116, v116
	v_exp_f32_e32 v117, v117
	v_exp_f32_e32 v118, v118
	v_exp_f32_e32 v119, v119
	v_pk_add_f32 v[152:153], v[152:153], v[112:113]
	v_pk_add_f32 v[154:155], v[154:155], v[114:115]
	v_pk_fma_f32 v[164:165], v[112:113], v[132:133], v[164:165] op_sel:[0,0,0] op_sel_hi:[1,0,1]
	v_pk_fma_f32 v[166:167], v[114:115], v[132:133], v[166:167] op_sel:[0,0,0] op_sel_hi:[1,0,1]
	v_pk_add_f32 v[152:153], v[152:153], v[116:117]
	v_pk_add_f32 v[154:155], v[154:155], v[118:119]
	v_pk_fma_f32 v[164:165], v[116:117], v[132:133], v[164:165] op_sel:[0,1,0] op_sel_hi:[1,1,1]
	v_pk_fma_f32 v[166:167], v[118:119], v[132:133], v[166:167] op_sel:[0,1,0] op_sel_hi:[1,1,1]
	v_pk_fma_f32 v[112:113], v[134:135], v[140:141], v[144:145] op_sel:[0,0,0] op_sel_hi:[0,1,1] neg_lo:[0,0,1] neg_hi:[0,0,1]
	v_pk_fma_f32 v[114:115], v[134:135], v[142:143], v[146:147] op_sel:[0,0,0] op_sel_hi:[0,1,1] neg_lo:[0,0,1] neg_hi:[0,0,1]
	v_exp_f32_e32 v112, v112
	v_exp_f32_e32 v113, v113
	v_exp_f32_e32 v114, v114
	v_exp_f32_e32 v115, v115
	v_pk_fma_f32 v[116:117], v[134:135], v[140:141], v[144:145] op_sel:[1,0,0] op_sel_hi:[1,1,1] neg_lo:[0,0,1] neg_hi:[0,0,1]
	v_pk_fma_f32 v[118:119], v[134:135], v[142:143], v[146:147] op_sel:[1,0,0] op_sel_hi:[1,1,1] neg_lo:[0,0,1] neg_hi:[0,0,1]
	v_exp_f32_e32 v116, v116
	v_exp_f32_e32 v117, v117
	v_exp_f32_e32 v118, v118
	v_exp_f32_e32 v119, v119
	v_pk_add_f32 v[152:153], v[152:153], v[112:113]
	v_pk_add_f32 v[154:155], v[154:155], v[114:115]
	v_pk_fma_f32 v[164:165], v[112:113], v[134:135], v[164:165] op_sel:[0,0,0] op_sel_hi:[1,0,1]
	v_pk_fma_f32 v[166:167], v[114:115], v[134:135], v[166:167] op_sel:[0,0,0] op_sel_hi:[1,0,1]
	v_pk_add_f32 v[152:153], v[152:153], v[116:117]
	v_pk_add_f32 v[154:155], v[154:155], v[118:119]
	v_pk_fma_f32 v[164:165], v[116:117], v[134:135], v[164:165] op_sel:[0,1,0] op_sel_hi:[1,1,1]
	v_pk_fma_f32 v[166:167], v[118:119], v[134:135], v[166:167] op_sel:[0,1,0] op_sel_hi:[1,1,1]
	v_pk_fma_f32 v[112:113], v[136:137], v[140:141], v[144:145] op_sel:[0,0,0] op_sel_hi:[0,1,1] neg_lo:[0,0,1] neg_hi:[0,0,1]
	v_pk_fma_f32 v[114:115], v[136:137], v[142:143], v[146:147] op_sel:[0,0,0] op_sel_hi:[0,1,1] neg_lo:[0,0,1] neg_hi:[0,0,1]
	v_exp_f32_e32 v112, v112
	v_exp_f32_e32 v113, v113
	v_exp_f32_e32 v114, v114
	v_exp_f32_e32 v115, v115
	v_pk_fma_f32 v[116:117], v[136:137], v[140:141], v[144:145] op_sel:[1,0,0] op_sel_hi:[1,1,1] neg_lo:[0,0,1] neg_hi:[0,0,1]
	v_pk_fma_f32 v[118:119], v[136:137], v[142:143], v[146:147] op_sel:[1,0,0] op_sel_hi:[1,1,1] neg_lo:[0,0,1] neg_hi:[0,0,1]
	v_exp_f32_e32 v116, v116
	v_exp_f32_e32 v117, v117
	v_exp_f32_e32 v118, v118
	v_exp_f32_e32 v119, v119
	v_pk_add_f32 v[152:153], v[152:153], v[112:113]
	v_pk_add_f32 v[154:155], v[154:155], v[114:115]
	v_pk_fma_f32 v[164:165], v[112:113], v[136:137], v[164:165] op_sel:[0,0,0] op_sel_hi:[1,0,1]
	v_pk_fma_f32 v[166:167], v[114:115], v[136:137], v[166:167] op_sel:[0,0,0] op_sel_hi:[1,0,1]
	v_pk_add_f32 v[152:153], v[152:153], v[116:117]
	v_pk_add_f32 v[154:155], v[154:155], v[118:119]
	v_pk_fma_f32 v[164:165], v[116:117], v[136:137], v[164:165] op_sel:[0,1,0] op_sel_hi:[1,1,1]
	v_pk_fma_f32 v[166:167], v[118:119], v[136:137], v[166:167] op_sel:[0,1,0] op_sel_hi:[1,1,1]
	v_pk_fma_f32 v[112:113], v[138:139], v[140:141], v[144:145] op_sel:[0,0,0] op_sel_hi:[0,1,1] neg_lo:[0,0,1] neg_hi:[0,0,1]
	v_pk_fma_f32 v[114:115], v[138:139], v[142:143], v[146:147] op_sel:[0,0,0] op_sel_hi:[0,1,1] neg_lo:[0,0,1] neg_hi:[0,0,1]
	v_exp_f32_e32 v112, v112
	v_exp_f32_e32 v113, v113
	v_exp_f32_e32 v114, v114
	v_exp_f32_e32 v115, v115
	v_pk_fma_f32 v[116:117], v[138:139], v[140:141], v[144:145] op_sel:[1,0,0] op_sel_hi:[1,1,1] neg_lo:[0,0,1] neg_hi:[0,0,1]
	v_pk_fma_f32 v[118:119], v[138:139], v[142:143], v[146:147] op_sel:[1,0,0] op_sel_hi:[1,1,1] neg_lo:[0,0,1] neg_hi:[0,0,1]
	v_exp_f32_e32 v116, v116
	v_exp_f32_e32 v117, v117
	v_exp_f32_e32 v118, v118
	v_exp_f32_e32 v119, v119
	v_pk_add_f32 v[152:153], v[152:153], v[112:113]
	v_pk_add_f32 v[154:155], v[154:155], v[114:115]
	v_pk_fma_f32 v[164:165], v[112:113], v[138:139], v[164:165] op_sel:[0,0,0] op_sel_hi:[1,0,1]
	v_pk_fma_f32 v[166:167], v[114:115], v[138:139], v[166:167] op_sel:[0,0,0] op_sel_hi:[1,0,1]
	v_pk_add_f32 v[152:153], v[152:153], v[116:117]
	v_pk_add_f32 v[154:155], v[154:155], v[118:119]
	v_pk_fma_f32 v[164:165], v[116:117], v[138:139], v[164:165] op_sel:[0,1,0] op_sel_hi:[1,1,1]
	v_pk_fma_f32 v[166:167], v[118:119], v[138:139], v[166:167] op_sel:[0,1,0] op_sel_hi:[1,1,1]
	v_pk_fma_f32 v[112:113], v[148:149], v[140:141], v[144:145] op_sel:[0,0,0] op_sel_hi:[0,1,1] neg_lo:[0,0,1] neg_hi:[0,0,1]
	v_pk_fma_f32 v[114:115], v[148:149], v[142:143], v[146:147] op_sel:[0,0,0] op_sel_hi:[0,1,1] neg_lo:[0,0,1] neg_hi:[0,0,1]
	v_exp_f32_e32 v112, v112
	v_exp_f32_e32 v113, v113
	v_exp_f32_e32 v114, v114
	v_exp_f32_e32 v115, v115
	v_pk_fma_f32 v[116:117], v[148:149], v[140:141], v[144:145] op_sel:[1,0,0] op_sel_hi:[1,1,1] neg_lo:[0,0,1] neg_hi:[0,0,1]
	v_pk_fma_f32 v[118:119], v[148:149], v[142:143], v[146:147] op_sel:[1,0,0] op_sel_hi:[1,1,1] neg_lo:[0,0,1] neg_hi:[0,0,1]
	v_exp_f32_e32 v116, v116
	v_exp_f32_e32 v117, v117
	v_exp_f32_e32 v118, v118
	v_exp_f32_e32 v119, v119
	v_pk_add_f32 v[152:153], v[152:153], v[112:113]
	v_pk_add_f32 v[154:155], v[154:155], v[114:115]
	v_pk_fma_f32 v[164:165], v[112:113], v[148:149], v[164:165] op_sel:[0,0,0] op_sel_hi:[1,0,1]
	v_pk_fma_f32 v[166:167], v[114:115], v[148:149], v[166:167] op_sel:[0,0,0] op_sel_hi:[1,0,1]
	v_pk_add_f32 v[152:153], v[152:153], v[116:117]
	v_pk_add_f32 v[154:155], v[154:155], v[118:119]
	v_pk_fma_f32 v[164:165], v[116:117], v[148:149], v[164:165] op_sel:[0,1,0] op_sel_hi:[1,1,1]
	v_pk_fma_f32 v[166:167], v[118:119], v[148:149], v[166:167] op_sel:[0,1,0] op_sel_hi:[1,1,1]
	v_pk_fma_f32 v[112:113], v[150:151], v[140:141], v[144:145] op_sel:[0,0,0] op_sel_hi:[0,1,1] neg_lo:[0,0,1] neg_hi:[0,0,1]
	v_pk_fma_f32 v[114:115], v[150:151], v[142:143], v[146:147] op_sel:[0,0,0] op_sel_hi:[0,1,1] neg_lo:[0,0,1] neg_hi:[0,0,1]
	v_exp_f32_e32 v112, v112
	v_exp_f32_e32 v113, v113
	v_exp_f32_e32 v114, v114
	v_exp_f32_e32 v115, v115
	v_pk_fma_f32 v[116:117], v[150:151], v[140:141], v[144:145] op_sel:[1,0,0] op_sel_hi:[1,1,1] neg_lo:[0,0,1] neg_hi:[0,0,1]
	v_pk_fma_f32 v[118:119], v[150:151], v[142:143], v[146:147] op_sel:[1,0,0] op_sel_hi:[1,1,1] neg_lo:[0,0,1] neg_hi:[0,0,1]
	v_exp_f32_e32 v116, v116
	v_exp_f32_e32 v117, v117
	v_exp_f32_e32 v118, v118
	v_exp_f32_e32 v119, v119
	v_pk_add_f32 v[152:153], v[152:153], v[112:113]
	v_pk_add_f32 v[154:155], v[154:155], v[114:115]
	v_pk_fma_f32 v[164:165], v[112:113], v[150:151], v[164:165] op_sel:[0,0,0] op_sel_hi:[1,0,1]
	v_pk_fma_f32 v[166:167], v[114:115], v[150:151], v[166:167] op_sel:[0,0,0] op_sel_hi:[1,0,1]
	v_pk_add_f32 v[152:153], v[152:153], v[116:117]
	v_pk_add_f32 v[154:155], v[154:155], v[118:119]
	v_pk_fma_f32 v[164:165], v[116:117], v[150:151], v[164:165] op_sel:[0,1,0] op_sel_hi:[1,1,1]
	v_pk_fma_f32 v[166:167], v[118:119], v[150:151], v[166:167] op_sel:[0,1,0] op_sel_hi:[1,1,1]
	v_pk_fma_f32 v[112:113], v[158:159], v[140:141], v[144:145] op_sel:[0,0,0] op_sel_hi:[0,1,1] neg_lo:[0,0,1] neg_hi:[0,0,1]
	v_pk_fma_f32 v[114:115], v[158:159], v[142:143], v[146:147] op_sel:[0,0,0] op_sel_hi:[0,1,1] neg_lo:[0,0,1] neg_hi:[0,0,1]
	v_exp_f32_e32 v112, v112
	v_exp_f32_e32 v113, v113
	v_exp_f32_e32 v114, v114
	v_exp_f32_e32 v115, v115
	v_pk_fma_f32 v[116:117], v[158:159], v[140:141], v[144:145] op_sel:[1,0,0] op_sel_hi:[1,1,1] neg_lo:[0,0,1] neg_hi:[0,0,1]
	v_pk_fma_f32 v[118:119], v[158:159], v[142:143], v[146:147] op_sel:[1,0,0] op_sel_hi:[1,1,1] neg_lo:[0,0,1] neg_hi:[0,0,1]
	v_exp_f32_e32 v116, v116
	v_exp_f32_e32 v117, v117
	v_exp_f32_e32 v118, v118
	v_exp_f32_e32 v119, v119
	v_pk_add_f32 v[152:153], v[152:153], v[112:113]
	v_pk_add_f32 v[154:155], v[154:155], v[114:115]
	v_pk_fma_f32 v[164:165], v[112:113], v[158:159], v[164:165] op_sel:[0,0,0] op_sel_hi:[1,0,1]
	v_pk_fma_f32 v[166:167], v[114:115], v[158:159], v[166:167] op_sel:[0,0,0] op_sel_hi:[1,0,1]
	v_pk_add_f32 v[152:153], v[152:153], v[116:117]
	v_pk_add_f32 v[154:155], v[154:155], v[118:119]
	v_pk_fma_f32 v[164:165], v[116:117], v[158:159], v[164:165] op_sel:[0,1,0] op_sel_hi:[1,1,1]
	v_pk_fma_f32 v[166:167], v[118:119], v[158:159], v[166:167] op_sel:[0,1,0] op_sel_hi:[1,1,1]
	v_pk_fma_f32 v[112:113], v[160:161], v[140:141], v[144:145] op_sel:[0,0,0] op_sel_hi:[0,1,1] neg_lo:[0,0,1] neg_hi:[0,0,1]
	v_pk_fma_f32 v[114:115], v[160:161], v[142:143], v[146:147] op_sel:[0,0,0] op_sel_hi:[0,1,1] neg_lo:[0,0,1] neg_hi:[0,0,1]
	v_exp_f32_e32 v112, v112
	v_exp_f32_e32 v113, v113
	v_exp_f32_e32 v114, v114
	v_exp_f32_e32 v115, v115
	v_pk_fma_f32 v[116:117], v[160:161], v[140:141], v[144:145] op_sel:[1,0,0] op_sel_hi:[1,1,1] neg_lo:[0,0,1] neg_hi:[0,0,1]
	v_pk_fma_f32 v[118:119], v[160:161], v[142:143], v[146:147] op_sel:[1,0,0] op_sel_hi:[1,1,1] neg_lo:[0,0,1] neg_hi:[0,0,1]
	v_exp_f32_e32 v116, v116
	v_exp_f32_e32 v117, v117
	v_exp_f32_e32 v118, v118
	v_exp_f32_e32 v119, v119
	v_pk_add_f32 v[152:153], v[152:153], v[112:113]
	v_pk_add_f32 v[154:155], v[154:155], v[114:115]
	v_pk_fma_f32 v[164:165], v[112:113], v[160:161], v[164:165] op_sel:[0,0,0] op_sel_hi:[1,0,1]
	v_pk_fma_f32 v[166:167], v[114:115], v[160:161], v[166:167] op_sel:[0,0,0] op_sel_hi:[1,0,1]
	v_pk_add_f32 v[152:153], v[152:153], v[116:117]
	v_pk_add_f32 v[154:155], v[154:155], v[118:119]
	v_pk_fma_f32 v[164:165], v[116:117], v[160:161], v[164:165] op_sel:[0,1,0] op_sel_hi:[1,1,1]
	v_pk_fma_f32 v[166:167], v[118:119], v[160:161], v[166:167] op_sel:[0,1,0] op_sel_hi:[1,1,1]
	v_pk_fma_f32 v[112:113], v[180:181], v[140:141], v[144:145] op_sel:[0,0,0] op_sel_hi:[0,1,1] neg_lo:[0,0,1] neg_hi:[0,0,1]
	v_pk_fma_f32 v[114:115], v[180:181], v[142:143], v[146:147] op_sel:[0,0,0] op_sel_hi:[0,1,1] neg_lo:[0,0,1] neg_hi:[0,0,1]
	v_exp_f32_e32 v112, v112
	v_exp_f32_e32 v113, v113
	v_exp_f32_e32 v114, v114
	v_exp_f32_e32 v115, v115
	v_pk_fma_f32 v[116:117], v[180:181], v[140:141], v[144:145] op_sel:[1,0,0] op_sel_hi:[1,1,1] neg_lo:[0,0,1] neg_hi:[0,0,1]
	v_pk_fma_f32 v[118:119], v[180:181], v[142:143], v[146:147] op_sel:[1,0,0] op_sel_hi:[1,1,1] neg_lo:[0,0,1] neg_hi:[0,0,1]
	v_exp_f32_e32 v116, v116
	v_exp_f32_e32 v117, v117
	v_exp_f32_e32 v118, v118
	v_exp_f32_e32 v119, v119
	v_pk_add_f32 v[152:153], v[152:153], v[112:113]
	v_pk_add_f32 v[154:155], v[154:155], v[114:115]
	v_pk_fma_f32 v[164:165], v[112:113], v[180:181], v[164:165] op_sel:[0,0,0] op_sel_hi:[1,0,1]
	v_pk_fma_f32 v[166:167], v[114:115], v[180:181], v[166:167] op_sel:[0,0,0] op_sel_hi:[1,0,1]
	v_pk_add_f32 v[152:153], v[152:153], v[116:117]
	v_pk_add_f32 v[154:155], v[154:155], v[118:119]
	v_pk_fma_f32 v[164:165], v[116:117], v[180:181], v[164:165] op_sel:[0,1,0] op_sel_hi:[1,1,1]
	v_pk_fma_f32 v[166:167], v[118:119], v[180:181], v[166:167] op_sel:[0,1,0] op_sel_hi:[1,1,1]
	v_pk_fma_f32 v[112:113], v[182:183], v[140:141], v[144:145] op_sel:[0,0,0] op_sel_hi:[0,1,1] neg_lo:[0,0,1] neg_hi:[0,0,1]
	v_pk_fma_f32 v[114:115], v[182:183], v[142:143], v[146:147] op_sel:[0,0,0] op_sel_hi:[0,1,1] neg_lo:[0,0,1] neg_hi:[0,0,1]
	v_exp_f32_e32 v112, v112
	v_exp_f32_e32 v113, v113
	v_exp_f32_e32 v114, v114
	v_exp_f32_e32 v115, v115
	v_pk_fma_f32 v[116:117], v[182:183], v[140:141], v[144:145] op_sel:[1,0,0] op_sel_hi:[1,1,1] neg_lo:[0,0,1] neg_hi:[0,0,1]
	v_pk_fma_f32 v[118:119], v[182:183], v[142:143], v[146:147] op_sel:[1,0,0] op_sel_hi:[1,1,1] neg_lo:[0,0,1] neg_hi:[0,0,1]
	v_exp_f32_e32 v116, v116
	v_exp_f32_e32 v117, v117
	v_exp_f32_e32 v118, v118
	v_exp_f32_e32 v119, v119
	v_pk_add_f32 v[152:153], v[152:153], v[112:113]
	v_pk_add_f32 v[154:155], v[154:155], v[114:115]
	v_pk_fma_f32 v[164:165], v[112:113], v[182:183], v[164:165] op_sel:[0,0,0] op_sel_hi:[1,0,1]
	v_pk_fma_f32 v[166:167], v[114:115], v[182:183], v[166:167] op_sel:[0,0,0] op_sel_hi:[1,0,1]
	v_pk_add_f32 v[152:153], v[152:153], v[116:117]
	v_pk_add_f32 v[154:155], v[154:155], v[118:119]
	v_pk_fma_f32 v[164:165], v[116:117], v[182:183], v[164:165] op_sel:[0,1,0] op_sel_hi:[1,1,1]
	v_pk_fma_f32 v[166:167], v[118:119], v[182:183], v[166:167] op_sel:[0,1,0] op_sel_hi:[1,1,1]
	s_waitcnt lgkmcnt(0)
	v_pk_fma_f32 v[112:113], v[68:69], v[140:141], v[144:145] op_sel:[0,0,0] op_sel_hi:[0,1,1] neg_lo:[0,0,1] neg_hi:[0,0,1]
	v_pk_fma_f32 v[114:115], v[68:69], v[142:143], v[146:147] op_sel:[0,0,0] op_sel_hi:[0,1,1] neg_lo:[0,0,1] neg_hi:[0,0,1]
	v_exp_f32_e32 v112, v112
	v_exp_f32_e32 v113, v113
	v_exp_f32_e32 v114, v114
	v_exp_f32_e32 v115, v115
	v_pk_fma_f32 v[116:117], v[68:69], v[140:141], v[144:145] op_sel:[1,0,0] op_sel_hi:[1,1,1] neg_lo:[0,0,1] neg_hi:[0,0,1]
	v_pk_fma_f32 v[118:119], v[68:69], v[142:143], v[146:147] op_sel:[1,0,0] op_sel_hi:[1,1,1] neg_lo:[0,0,1] neg_hi:[0,0,1]
	v_exp_f32_e32 v116, v116
	v_exp_f32_e32 v117, v117
	v_exp_f32_e32 v118, v118
	v_exp_f32_e32 v119, v119
	v_pk_add_f32 v[152:153], v[152:153], v[112:113]
	v_pk_add_f32 v[154:155], v[154:155], v[114:115]
	v_pk_fma_f32 v[164:165], v[112:113], v[68:69], v[164:165] op_sel:[0,0,0] op_sel_hi:[1,0,1]
	v_pk_fma_f32 v[166:167], v[114:115], v[68:69], v[166:167] op_sel:[0,0,0] op_sel_hi:[1,0,1]
	v_pk_add_f32 v[152:153], v[152:153], v[116:117]
	v_pk_add_f32 v[154:155], v[154:155], v[118:119]
	v_pk_fma_f32 v[164:165], v[116:117], v[68:69], v[164:165] op_sel:[0,1,0] op_sel_hi:[1,1,1]
	v_pk_fma_f32 v[166:167], v[118:119], v[68:69], v[166:167] op_sel:[0,1,0] op_sel_hi:[1,1,1]
	v_pk_fma_f32 v[112:113], v[70:71], v[140:141], v[144:145] op_sel:[0,0,0] op_sel_hi:[0,1,1] neg_lo:[0,0,1] neg_hi:[0,0,1]
	v_pk_fma_f32 v[114:115], v[70:71], v[142:143], v[146:147] op_sel:[0,0,0] op_sel_hi:[0,1,1] neg_lo:[0,0,1] neg_hi:[0,0,1]
	v_exp_f32_e32 v112, v112
	v_exp_f32_e32 v113, v113
	v_exp_f32_e32 v114, v114
	v_exp_f32_e32 v115, v115
	v_pk_fma_f32 v[116:117], v[70:71], v[140:141], v[144:145] op_sel:[1,0,0] op_sel_hi:[1,1,1] neg_lo:[0,0,1] neg_hi:[0,0,1]
	v_pk_fma_f32 v[118:119], v[70:71], v[142:143], v[146:147] op_sel:[1,0,0] op_sel_hi:[1,1,1] neg_lo:[0,0,1] neg_hi:[0,0,1]
	v_exp_f32_e32 v116, v116
	v_exp_f32_e32 v117, v117
	v_exp_f32_e32 v118, v118
	v_exp_f32_e32 v119, v119
	v_pk_add_f32 v[152:153], v[152:153], v[112:113]
	v_pk_add_f32 v[154:155], v[154:155], v[114:115]
	v_pk_fma_f32 v[164:165], v[112:113], v[70:71], v[164:165] op_sel:[0,0,0] op_sel_hi:[1,0,1]
	v_pk_fma_f32 v[166:167], v[114:115], v[70:71], v[166:167] op_sel:[0,0,0] op_sel_hi:[1,0,1]
	v_pk_add_f32 v[152:153], v[152:153], v[116:117]
	v_pk_add_f32 v[154:155], v[154:155], v[118:119]
	v_pk_fma_f32 v[164:165], v[116:117], v[70:71], v[164:165] op_sel:[0,1,0] op_sel_hi:[1,1,1]
	v_pk_fma_f32 v[166:167], v[118:119], v[70:71], v[166:167] op_sel:[0,1,0] op_sel_hi:[1,1,1]
	v_pk_fma_f32 v[112:113], v[92:93], v[140:141], v[144:145] op_sel:[0,0,0] op_sel_hi:[0,1,1] neg_lo:[0,0,1] neg_hi:[0,0,1]
	v_pk_fma_f32 v[114:115], v[92:93], v[142:143], v[146:147] op_sel:[0,0,0] op_sel_hi:[0,1,1] neg_lo:[0,0,1] neg_hi:[0,0,1]
	v_exp_f32_e32 v112, v112
	v_exp_f32_e32 v113, v113
	v_exp_f32_e32 v114, v114
	v_exp_f32_e32 v115, v115
	v_pk_fma_f32 v[116:117], v[92:93], v[140:141], v[144:145] op_sel:[1,0,0] op_sel_hi:[1,1,1] neg_lo:[0,0,1] neg_hi:[0,0,1]
	v_pk_fma_f32 v[118:119], v[92:93], v[142:143], v[146:147] op_sel:[1,0,0] op_sel_hi:[1,1,1] neg_lo:[0,0,1] neg_hi:[0,0,1]
	v_exp_f32_e32 v116, v116
	v_exp_f32_e32 v117, v117
	v_exp_f32_e32 v118, v118
	v_exp_f32_e32 v119, v119
	v_pk_add_f32 v[152:153], v[152:153], v[112:113]
	v_pk_add_f32 v[154:155], v[154:155], v[114:115]
	v_pk_fma_f32 v[164:165], v[112:113], v[92:93], v[164:165] op_sel:[0,0,0] op_sel_hi:[1,0,1]
	v_pk_fma_f32 v[166:167], v[114:115], v[92:93], v[166:167] op_sel:[0,0,0] op_sel_hi:[1,0,1]
	v_pk_add_f32 v[152:153], v[152:153], v[116:117]
	v_pk_add_f32 v[154:155], v[154:155], v[118:119]
	v_pk_fma_f32 v[164:165], v[116:117], v[92:93], v[164:165] op_sel:[0,1,0] op_sel_hi:[1,1,1]
	v_pk_fma_f32 v[166:167], v[118:119], v[92:93], v[166:167] op_sel:[0,1,0] op_sel_hi:[1,1,1]
	v_pk_fma_f32 v[112:113], v[94:95], v[140:141], v[144:145] op_sel:[0,0,0] op_sel_hi:[0,1,1] neg_lo:[0,0,1] neg_hi:[0,0,1]
	v_pk_fma_f32 v[114:115], v[94:95], v[142:143], v[146:147] op_sel:[0,0,0] op_sel_hi:[0,1,1] neg_lo:[0,0,1] neg_hi:[0,0,1]
	v_exp_f32_e32 v112, v112
	v_exp_f32_e32 v113, v113
	v_exp_f32_e32 v114, v114
	v_exp_f32_e32 v115, v115
	v_pk_fma_f32 v[116:117], v[94:95], v[140:141], v[144:145] op_sel:[1,0,0] op_sel_hi:[1,1,1] neg_lo:[0,0,1] neg_hi:[0,0,1]
	v_pk_fma_f32 v[118:119], v[94:95], v[142:143], v[146:147] op_sel:[1,0,0] op_sel_hi:[1,1,1] neg_lo:[0,0,1] neg_hi:[0,0,1]
	v_exp_f32_e32 v116, v116
	v_exp_f32_e32 v117, v117
	v_exp_f32_e32 v118, v118
	v_exp_f32_e32 v119, v119
	v_pk_add_f32 v[152:153], v[152:153], v[112:113]
	v_pk_add_f32 v[154:155], v[154:155], v[114:115]
	v_pk_fma_f32 v[164:165], v[112:113], v[94:95], v[164:165] op_sel:[0,0,0] op_sel_hi:[1,0,1]
	v_pk_fma_f32 v[166:167], v[114:115], v[94:95], v[166:167] op_sel:[0,0,0] op_sel_hi:[1,0,1]
	v_pk_add_f32 v[152:153], v[152:153], v[116:117]
	v_pk_add_f32 v[154:155], v[154:155], v[118:119]
	v_pk_fma_f32 v[164:165], v[116:117], v[94:95], v[164:165] op_sel:[0,1,0] op_sel_hi:[1,1,1]
	v_pk_fma_f32 v[166:167], v[118:119], v[94:95], v[166:167] op_sel:[0,1,0] op_sel_hi:[1,1,1]
	v_pk_fma_f32 v[112:113], v[100:101], v[140:141], v[144:145] op_sel:[0,0,0] op_sel_hi:[0,1,1] neg_lo:[0,0,1] neg_hi:[0,0,1]
	v_pk_fma_f32 v[114:115], v[100:101], v[142:143], v[146:147] op_sel:[0,0,0] op_sel_hi:[0,1,1] neg_lo:[0,0,1] neg_hi:[0,0,1]
	v_exp_f32_e32 v112, v112
	v_exp_f32_e32 v113, v113
	v_exp_f32_e32 v114, v114
	v_exp_f32_e32 v115, v115
	v_pk_fma_f32 v[116:117], v[100:101], v[140:141], v[144:145] op_sel:[1,0,0] op_sel_hi:[1,1,1] neg_lo:[0,0,1] neg_hi:[0,0,1]
	v_pk_fma_f32 v[118:119], v[100:101], v[142:143], v[146:147] op_sel:[1,0,0] op_sel_hi:[1,1,1] neg_lo:[0,0,1] neg_hi:[0,0,1]
	v_exp_f32_e32 v116, v116
	v_exp_f32_e32 v117, v117
	v_exp_f32_e32 v118, v118
	v_exp_f32_e32 v119, v119
	v_pk_add_f32 v[152:153], v[152:153], v[112:113]
	v_pk_add_f32 v[154:155], v[154:155], v[114:115]
	v_pk_fma_f32 v[164:165], v[112:113], v[100:101], v[164:165] op_sel:[0,0,0] op_sel_hi:[1,0,1]
	v_pk_fma_f32 v[166:167], v[114:115], v[100:101], v[166:167] op_sel:[0,0,0] op_sel_hi:[1,0,1]
	v_pk_add_f32 v[152:153], v[152:153], v[116:117]
	v_pk_add_f32 v[154:155], v[154:155], v[118:119]
	v_pk_fma_f32 v[164:165], v[116:117], v[100:101], v[164:165] op_sel:[0,1,0] op_sel_hi:[1,1,1]
	v_pk_fma_f32 v[166:167], v[118:119], v[100:101], v[166:167] op_sel:[0,1,0] op_sel_hi:[1,1,1]
	v_pk_fma_f32 v[112:113], v[102:103], v[140:141], v[144:145] op_sel:[0,0,0] op_sel_hi:[0,1,1] neg_lo:[0,0,1] neg_hi:[0,0,1]
	v_pk_fma_f32 v[114:115], v[102:103], v[142:143], v[146:147] op_sel:[0,0,0] op_sel_hi:[0,1,1] neg_lo:[0,0,1] neg_hi:[0,0,1]
	v_exp_f32_e32 v112, v112
	v_exp_f32_e32 v113, v113
	v_exp_f32_e32 v114, v114
	v_exp_f32_e32 v115, v115
	v_pk_fma_f32 v[116:117], v[102:103], v[140:141], v[144:145] op_sel:[1,0,0] op_sel_hi:[1,1,1] neg_lo:[0,0,1] neg_hi:[0,0,1]
	v_pk_fma_f32 v[118:119], v[102:103], v[142:143], v[146:147] op_sel:[1,0,0] op_sel_hi:[1,1,1] neg_lo:[0,0,1] neg_hi:[0,0,1]
	v_exp_f32_e32 v116, v116
	v_exp_f32_e32 v117, v117
	v_exp_f32_e32 v118, v118
	v_exp_f32_e32 v119, v119
	v_pk_add_f32 v[152:153], v[152:153], v[112:113]
	v_pk_add_f32 v[154:155], v[154:155], v[114:115]
	v_pk_fma_f32 v[164:165], v[112:113], v[102:103], v[164:165] op_sel:[0,0,0] op_sel_hi:[1,0,1]
	v_pk_fma_f32 v[166:167], v[114:115], v[102:103], v[166:167] op_sel:[0,0,0] op_sel_hi:[1,0,1]
	v_pk_add_f32 v[152:153], v[152:153], v[116:117]
	v_pk_add_f32 v[154:155], v[154:155], v[118:119]
	v_pk_fma_f32 v[164:165], v[116:117], v[102:103], v[164:165] op_sel:[0,1,0] op_sel_hi:[1,1,1]
	v_pk_fma_f32 v[166:167], v[118:119], v[102:103], v[166:167] op_sel:[0,1,0] op_sel_hi:[1,1,1]
	v_pk_fma_f32 v[112:113], v[104:105], v[140:141], v[144:145] op_sel:[0,0,0] op_sel_hi:[0,1,1] neg_lo:[0,0,1] neg_hi:[0,0,1]
	v_pk_fma_f32 v[114:115], v[104:105], v[142:143], v[146:147] op_sel:[0,0,0] op_sel_hi:[0,1,1] neg_lo:[0,0,1] neg_hi:[0,0,1]
	v_exp_f32_e32 v112, v112
	v_exp_f32_e32 v113, v113
	v_exp_f32_e32 v114, v114
	v_exp_f32_e32 v115, v115
	v_pk_fma_f32 v[116:117], v[104:105], v[140:141], v[144:145] op_sel:[1,0,0] op_sel_hi:[1,1,1] neg_lo:[0,0,1] neg_hi:[0,0,1]
	v_pk_fma_f32 v[118:119], v[104:105], v[142:143], v[146:147] op_sel:[1,0,0] op_sel_hi:[1,1,1] neg_lo:[0,0,1] neg_hi:[0,0,1]
	v_exp_f32_e32 v116, v116
	v_exp_f32_e32 v117, v117
	v_exp_f32_e32 v118, v118
	v_exp_f32_e32 v119, v119
	v_pk_add_f32 v[152:153], v[152:153], v[112:113]
	v_pk_add_f32 v[154:155], v[154:155], v[114:115]
	v_pk_fma_f32 v[164:165], v[112:113], v[104:105], v[164:165] op_sel:[0,0,0] op_sel_hi:[1,0,1]
	v_pk_fma_f32 v[166:167], v[114:115], v[104:105], v[166:167] op_sel:[0,0,0] op_sel_hi:[1,0,1]
	v_pk_add_f32 v[152:153], v[152:153], v[116:117]
	v_pk_add_f32 v[154:155], v[154:155], v[118:119]
	v_pk_fma_f32 v[164:165], v[116:117], v[104:105], v[164:165] op_sel:[0,1,0] op_sel_hi:[1,1,1]
	v_pk_fma_f32 v[166:167], v[118:119], v[104:105], v[166:167] op_sel:[0,1,0] op_sel_hi:[1,1,1]
	v_pk_fma_f32 v[112:113], v[106:107], v[140:141], v[144:145] op_sel:[0,0,0] op_sel_hi:[0,1,1] neg_lo:[0,0,1] neg_hi:[0,0,1]
	v_pk_fma_f32 v[114:115], v[106:107], v[142:143], v[146:147] op_sel:[0,0,0] op_sel_hi:[0,1,1] neg_lo:[0,0,1] neg_hi:[0,0,1]
	v_exp_f32_e32 v112, v112
	v_exp_f32_e32 v113, v113
	v_exp_f32_e32 v114, v114
	v_exp_f32_e32 v115, v115
	v_pk_fma_f32 v[116:117], v[106:107], v[140:141], v[144:145] op_sel:[1,0,0] op_sel_hi:[1,1,1] neg_lo:[0,0,1] neg_hi:[0,0,1]
	v_pk_fma_f32 v[118:119], v[106:107], v[142:143], v[146:147] op_sel:[1,0,0] op_sel_hi:[1,1,1] neg_lo:[0,0,1] neg_hi:[0,0,1]
	v_exp_f32_e32 v116, v116
	v_exp_f32_e32 v117, v117
	v_exp_f32_e32 v118, v118
	v_exp_f32_e32 v119, v119
	v_pk_add_f32 v[152:153], v[152:153], v[112:113]
	v_pk_add_f32 v[154:155], v[154:155], v[114:115]
	v_pk_fma_f32 v[164:165], v[112:113], v[106:107], v[164:165] op_sel:[0,0,0] op_sel_hi:[1,0,1]
	v_pk_fma_f32 v[166:167], v[114:115], v[106:107], v[166:167] op_sel:[0,0,0] op_sel_hi:[1,0,1]
	v_pk_add_f32 v[152:153], v[152:153], v[116:117]
	v_pk_add_f32 v[154:155], v[154:155], v[118:119]
	v_pk_fma_f32 v[164:165], v[116:117], v[106:107], v[164:165] op_sel:[0,1,0] op_sel_hi:[1,1,1]
	v_pk_fma_f32 v[166:167], v[118:119], v[106:107], v[166:167] op_sel:[0,1,0] op_sel_hi:[1,1,1]
	v_pk_fma_f32 v[112:113], v[108:109], v[140:141], v[144:145] op_sel:[0,0,0] op_sel_hi:[0,1,1] neg_lo:[0,0,1] neg_hi:[0,0,1]
	v_pk_fma_f32 v[114:115], v[108:109], v[142:143], v[146:147] op_sel:[0,0,0] op_sel_hi:[0,1,1] neg_lo:[0,0,1] neg_hi:[0,0,1]
	v_exp_f32_e32 v112, v112
	v_exp_f32_e32 v113, v113
	v_exp_f32_e32 v114, v114
	v_exp_f32_e32 v115, v115
	v_pk_fma_f32 v[116:117], v[108:109], v[140:141], v[144:145] op_sel:[1,0,0] op_sel_hi:[1,1,1] neg_lo:[0,0,1] neg_hi:[0,0,1]
	v_pk_fma_f32 v[118:119], v[108:109], v[142:143], v[146:147] op_sel:[1,0,0] op_sel_hi:[1,1,1] neg_lo:[0,0,1] neg_hi:[0,0,1]
	v_exp_f32_e32 v116, v116
	v_exp_f32_e32 v117, v117
	v_exp_f32_e32 v118, v118
	v_exp_f32_e32 v119, v119
	v_pk_add_f32 v[152:153], v[152:153], v[112:113]
	v_pk_add_f32 v[154:155], v[154:155], v[114:115]
	v_pk_fma_f32 v[164:165], v[112:113], v[108:109], v[164:165] op_sel:[0,0,0] op_sel_hi:[1,0,1]
	v_pk_fma_f32 v[166:167], v[114:115], v[108:109], v[166:167] op_sel:[0,0,0] op_sel_hi:[1,0,1]
	v_pk_add_f32 v[152:153], v[152:153], v[116:117]
	v_pk_add_f32 v[154:155], v[154:155], v[118:119]
	v_pk_fma_f32 v[164:165], v[116:117], v[108:109], v[164:165] op_sel:[0,1,0] op_sel_hi:[1,1,1]
	v_pk_fma_f32 v[166:167], v[118:119], v[108:109], v[166:167] op_sel:[0,1,0] op_sel_hi:[1,1,1]
	v_pk_fma_f32 v[112:113], v[110:111], v[140:141], v[144:145] op_sel:[0,0,0] op_sel_hi:[0,1,1] neg_lo:[0,0,1] neg_hi:[0,0,1]
	v_pk_fma_f32 v[114:115], v[110:111], v[142:143], v[146:147] op_sel:[0,0,0] op_sel_hi:[0,1,1] neg_lo:[0,0,1] neg_hi:[0,0,1]
	v_exp_f32_e32 v112, v112
	v_exp_f32_e32 v113, v113
	v_exp_f32_e32 v114, v114
	v_exp_f32_e32 v115, v115
	v_pk_fma_f32 v[116:117], v[110:111], v[140:141], v[144:145] op_sel:[1,0,0] op_sel_hi:[1,1,1] neg_lo:[0,0,1] neg_hi:[0,0,1]
	v_pk_fma_f32 v[118:119], v[110:111], v[142:143], v[146:147] op_sel:[1,0,0] op_sel_hi:[1,1,1] neg_lo:[0,0,1] neg_hi:[0,0,1]
	v_exp_f32_e32 v116, v116
	v_exp_f32_e32 v117, v117
	v_exp_f32_e32 v118, v118
	v_exp_f32_e32 v119, v119
	v_pk_add_f32 v[152:153], v[152:153], v[112:113]
	v_pk_add_f32 v[154:155], v[154:155], v[114:115]
	v_pk_fma_f32 v[164:165], v[112:113], v[110:111], v[164:165] op_sel:[0,0,0] op_sel_hi:[1,0,1]
	v_pk_fma_f32 v[166:167], v[114:115], v[110:111], v[166:167] op_sel:[0,0,0] op_sel_hi:[1,0,1]
	v_pk_add_f32 v[152:153], v[152:153], v[116:117]
	v_pk_add_f32 v[154:155], v[154:155], v[118:119]
	v_pk_fma_f32 v[164:165], v[116:117], v[110:111], v[164:165] op_sel:[0,1,0] op_sel_hi:[1,1,1]
	v_pk_fma_f32 v[166:167], v[118:119], v[110:111], v[166:167] op_sel:[0,1,0] op_sel_hi:[1,1,1]
	v_mov_b32_e32 v73, v164
	v_mov_b32_e32 v56, v165
	v_mov_b32_e32 v48, v166
	v_mov_b32_e32 v9, v167
	s_waitcnt lgkmcnt(0)
	s_waitcnt lgkmcnt(0)
	s_waitcnt lgkmcnt(0)
	ds_read_b128 v[128:131], v99 offset:1600
	ds_read_b128 v[182:185], v99 offset:1632
	s_waitcnt lgkmcnt(0)
	v_pk_add_f32 v[186:187], v[128:129], v[44:45]
	v_mov_b32_e32 v4, v152
	v_and_b32_e32 v0, 32, v0
	v_mov_b32_e32 v44, v4
	v_mov_b32_e32 v45, v4
	s_nop 1
	v_permlane32_swap_b32_e32 v44, v45
	v_cmp_eq_u32_e32 vcc, 0, v0
	v_mov_b32_e32 v83, v73
	v_pk_add_f32 v[188:189], v[130:131], v[46:47]
	v_cndmask_b32_e32 v0, v44, v45, vcc
	v_add_f32_e32 v0, v4, v0
	v_mov_b32_e32 v4, v73
	v_rcp_f32_e32 v0, v0
	s_nop 0
	v_permlane32_swap_b32_e32 v4, v83
	v_cndmask_b32_e32 v4, v4, v83, vcc
	v_add_f32_e32 v4, v73, v4
	v_mul_f32_e32 v0, v4, v0
	ds_read_b128 v[44:47], v99 offset:576
	ds_read_b128 v[128:131], v99 offset:608
	v_mov_b32_e32 v4, v153
	s_waitcnt lgkmcnt(0)
	v_pk_fma_f32 v[186:187], v[0:1], v[44:45], v[186:187] op_sel_hi:[0,1,1]
	v_mov_b32_e32 v8, v4
	v_mov_b32_e32 v44, v4
	s_nop 1
	v_permlane32_swap_b32_e32 v8, v44
	v_cndmask_b32_e32 v8, v8, v44, vcc
	v_add_f32_e32 v4, v4, v8
	v_mov_b32_e32 v8, v56
	v_mov_b32_e32 v67, v56
	v_rcp_f32_e32 v4, v4
	s_nop 0
	v_permlane32_swap_b32_e32 v8, v67
	v_cndmask_b32_e32 v8, v8, v67, vcc
	v_add_f32_e32 v8, v56, v8
	v_mul_f32_e32 v4, v8, v4
	v_pk_fma_f32 v[188:189], v[0:1], v[46:47], v[188:189] op_sel_hi:[0,1,1]
	ds_read_b128 v[44:47], v99 offset:832
	ds_read_b128 v[120:123], v99 offset:864
	v_mov_b32_e32 v8, v154
	s_waitcnt lgkmcnt(0)
	v_pk_fma_f32 v[84:85], v[4:5], v[44:45], v[186:187] op_sel_hi:[0,1,1]
	v_mov_b32_e32 v12, v8
	v_mov_b32_e32 v44, v8
	s_nop 1
	v_permlane32_swap_b32_e32 v12, v44
	v_cndmask_b32_e32 v12, v12, v44, vcc
	v_add_f32_e32 v8, v8, v12
	v_mov_b32_e32 v12, v48
	v_mov_b32_e32 v53, v48
	v_rcp_f32_e32 v8, v8
	s_nop 0
	v_permlane32_swap_b32_e32 v12, v53
	v_cndmask_b32_e32 v12, v12, v53, vcc
	v_add_f32_e32 v12, v48, v12
	v_mul_f32_e32 v62, v12, v8
	v_pk_fma_f32 v[90:91], v[4:5], v[46:47], v[188:189] op_sel_hi:[0,1,1]
	ds_read_b128 v[44:47], v99 offset:1088
	ds_read_b128 v[76:79], v99 offset:1120
	v_pk_add_f32 v[40:41], v[182:183], v[40:41]
	v_pk_add_f32 v[42:43], v[184:185], v[42:43]
	v_pk_fma_f32 v[40:41], v[0:1], v[128:129], v[40:41] op_sel_hi:[0,1,1]
	v_pk_fma_f32 v[42:43], v[0:1], v[130:131], v[42:43] op_sel_hi:[0,1,1]
	s_waitcnt lgkmcnt(0)
	v_pk_fma_f32 v[56:57], v[62:63], v[44:45], v[84:85] op_sel_hi:[0,1,1]
	v_pk_fma_f32 v[66:67], v[62:63], v[46:47], v[90:91] op_sel_hi:[0,1,1]
	v_pk_fma_f32 v[44:45], v[4:5], v[120:121], v[40:41] op_sel_hi:[0,1,1]
	v_pk_fma_f32 v[46:47], v[4:5], v[122:123], v[42:43] op_sel_hi:[0,1,1]
	ds_read_b128 v[40:43], v99 offset:1664
	v_pk_fma_f32 v[72:73], v[62:63], v[76:77], v[44:45] op_sel_hi:[0,1,1]
	v_pk_fma_f32 v[84:85], v[62:63], v[78:79], v[46:47] op_sel_hi:[0,1,1]
	ds_read_b128 v[44:47], v99 offset:1696
	ds_read_b128 v[76:79], v99 offset:640
	s_waitcnt lgkmcnt(0)
	v_pk_add_f32 v[80:81], v[40:41], v[36:37]
	v_pk_add_f32 v[82:83], v[42:43], v[38:39]
	ds_read_b128 v[36:39], v99 offset:672
	ds_read_b128 v[40:43], v99 offset:896
	v_pk_fma_f32 v[86:87], v[0:1], v[76:77], v[80:81] op_sel_hi:[0,1,1]
	v_pk_fma_f32 v[90:91], v[0:1], v[78:79], v[82:83] op_sel_hi:[0,1,1]
	ds_read_b128 v[76:79], v99 offset:1152
	ds_read_b128 v[80:83], v99 offset:928
	s_waitcnt lgkmcnt(0)
	v_pk_fma_f32 v[86:87], v[4:5], v[40:41], v[86:87] op_sel_hi:[0,1,1]
	v_pk_fma_f32 v[90:91], v[4:5], v[42:43], v[90:91] op_sel_hi:[0,1,1]
	ds_read_b128 v[40:43], v99 offset:1184
	v_pk_add_f32 v[32:33], v[44:45], v[32:33]
	v_pk_add_f32 v[34:35], v[46:47], v[34:35]
	v_pk_fma_f32 v[32:33], v[0:1], v[36:37], v[32:33] op_sel_hi:[0,1,1]
	v_pk_fma_f32 v[34:35], v[0:1], v[38:39], v[34:35] op_sel_hi:[0,1,1]
	v_pk_fma_f32 v[36:37], v[4:5], v[80:81], v[32:33] op_sel_hi:[0,1,1]
	v_pk_fma_f32 v[38:39], v[4:5], v[82:83], v[34:35] op_sel_hi:[0,1,1]
	ds_read_b128 v[32:35], v99 offset:1728
	s_waitcnt lgkmcnt(0)
	v_pk_fma_f32 v[80:81], v[62:63], v[40:41], v[36:37] op_sel_hi:[0,1,1]
	v_pk_fma_f32 v[82:83], v[62:63], v[42:43], v[38:39] op_sel_hi:[0,1,1]
	ds_read_b128 v[36:39], v99 offset:1760
	ds_read_b128 v[40:43], v99 offset:704
	v_mov_b32_e32 v8, v155
	v_pk_add_f32 v[44:45], v[32:33], v[28:29]
	v_pk_add_f32 v[46:47], v[34:35], v[30:31]
	ds_read_b128 v[28:31], v99 offset:736
	ds_read_b128 v[32:35], v99 offset:960
	v_mov_b32_e32 v10, v8
	v_mov_b32_e32 v11, v8
	s_nop 1
	v_permlane32_swap_b32_e32 v10, v11
	v_cndmask_b32_e32 v10, v10, v11, vcc
	v_pk_fma_f32 v[76:77], v[62:63], v[76:77], v[86:87] op_sel_hi:[0,1,1]
	v_pk_fma_f32 v[78:79], v[62:63], v[78:79], v[90:91] op_sel_hi:[0,1,1]
	s_waitcnt lgkmcnt(0)
	v_pk_fma_f32 v[86:87], v[0:1], v[40:41], v[44:45] op_sel_hi:[0,1,1]
	v_pk_fma_f32 v[90:91], v[0:1], v[42:43], v[46:47] op_sel_hi:[0,1,1]
	ds_read_b128 v[40:43], v99 offset:1216
	ds_read_b128 v[44:47], v99 offset:992
	v_add_f32_e32 v8, v8, v10
	v_mov_b32_e32 v10, v9
	v_mov_b32_e32 v11, v9
	s_nop 1
	v_permlane32_swap_b32_e32 v10, v11
	v_pk_fma_f32 v[86:87], v[4:5], v[32:33], v[86:87] op_sel_hi:[0,1,1]
	v_pk_fma_f32 v[90:91], v[4:5], v[34:35], v[90:91] op_sel_hi:[0,1,1]
	ds_read_b128 v[32:35], v99 offset:1248
	v_rcp_f32_e32 v8, v8
	v_cndmask_b32_e32 v14, v10, v11, vcc
	ds_read_b128 v[10:13], v99 offset:1344
	s_waitcnt lgkmcnt(0)
	v_pk_fma_f32 v[86:87], v[62:63], v[40:41], v[86:87] op_sel_hi:[0,1,1]
	v_pk_fma_f32 v[90:91], v[62:63], v[42:43], v[90:91] op_sel_hi:[0,1,1]
	v_add_f32_e32 v9, v9, v14
	ds_read_b128 v[14:17], v99 offset:1824
	ds_read_b128 v[40:43], v99 offset:1376
	v_mul_f32_e32 v60, v9, v8
	v_pk_fma_f32 v[68:69], v[60:61], v[10:11], v[56:57] op_sel_hi:[0,1,1]
	ds_read_b128 v[8:11], v99 offset:800
	s_waitcnt lgkmcnt(0)
	v_pk_add_f32 v[26:27], v[16:17], v[26:27]
	ds_read_b128 v[16:19], v99 offset:1056
	ds_read_b128 v[48:51], v99 offset:1792
	v_pk_fma_f32 v[66:67], v[60:61], v[12:13], v[66:67] op_sel_hi:[0,1,1]
	v_pk_add_f32 v[22:23], v[14:15], v[22:23]
	ds_read_b128 v[12:15], v99 offset:768
	v_pk_fma_f32 v[26:27], v[0:1], v[10:11], v[26:27] op_sel_hi:[0,1,1]
	v_pk_fma_f32 v[22:23], v[0:1], v[8:9], v[22:23] op_sel_hi:[0,1,1]
	ds_read_b128 v[8:11], v99 offset:1024
	ds_read_b128 v[52:55], v99 offset:1312
	s_waitcnt lgkmcnt(0)
	v_pk_fma_f32 v[26:27], v[4:5], v[18:19], v[26:27] op_sel_hi:[0,1,1]
	v_pk_fma_f32 v[22:23], v[4:5], v[16:17], v[22:23] op_sel_hi:[0,1,1]
	ds_read_b128 v[16:19], v99 offset:1280
	v_pk_add_f32 v[2:3], v[48:49], v[2:3]
	v_pk_add_f32 v[20:21], v[50:51], v[20:21]
	v_pk_fma_f32 v[2:3], v[0:1], v[12:13], v[2:3] op_sel_hi:[0,1,1]
	v_pk_fma_f32 v[2:3], v[4:5], v[8:9], v[2:3] op_sel_hi:[0,1,1]
	s_waitcnt lgkmcnt(0)
	v_pk_fma_f32 v[12:13], v[62:63], v[16:17], v[2:3] op_sel_hi:[0,1,1]
	v_pk_add_f32 v[2:3], v[36:37], v[6:7]
	v_pk_add_f32 v[6:7], v[38:39], v[24:25]
	v_pk_fma_f32 v[14:15], v[0:1], v[14:15], v[20:21] op_sel_hi:[0,1,1]
	v_pk_fma_f32 v[2:3], v[0:1], v[28:29], v[2:3] op_sel_hi:[0,1,1]
	v_pk_fma_f32 v[6:7], v[0:1], v[30:31], v[6:7] op_sel_hi:[0,1,1]
	v_add_f32_e32 v0, 0, v68
	v_add_f32_e32 v0, v69, v0
	v_pk_fma_f32 v[10:11], v[4:5], v[10:11], v[14:15] op_sel_hi:[0,1,1]
	v_pk_fma_f32 v[14:15], v[4:5], v[44:45], v[2:3] op_sel_hi:[0,1,1]
	v_pk_fma_f32 v[16:17], v[4:5], v[46:47], v[6:7] op_sel_hi:[0,1,1]
	v_add_f32_e32 v0, v66, v0
	ds_read_b128 v[56:59], v99 offset:1568
	v_pk_fma_f32 v[26:27], v[62:63], v[54:55], v[26:27] op_sel_hi:[0,1,1]
	v_pk_fma_f32 v[22:23], v[62:63], v[52:53], v[22:23] op_sel_hi:[0,1,1]
	ds_read_b128 v[52:55], v99 offset:1536
	v_lshlrev_b32_e32 v100, 2, v5
	ds_read_b128 v[2:5], v99 offset:1408
	ds_read_b128 v[6:9], v99 offset:1440
	v_pk_fma_f32 v[24:25], v[62:63], v[32:33], v[14:15] op_sel_hi:[0,1,1]
	v_pk_fma_f32 v[32:33], v[62:63], v[34:35], v[16:17] op_sel_hi:[0,1,1]
	v_pk_fma_f32 v[34:35], v[60:61], v[40:41], v[72:73] op_sel_hi:[0,1,1]
	v_add_f32_e32 v0, v67, v0
	v_add_f32_e32 v0, v34, v0
	v_pk_fma_f32 v[36:37], v[60:61], v[42:43], v[84:85] op_sel_hi:[0,1,1]
	v_add_f32_e32 v0, v35, v0
	v_add_f32_e32 v0, v36, v0
	v_add_f32_e32 v0, v37, v0
	s_waitcnt lgkmcnt(0)
	v_pk_fma_f32 v[2:3], v[60:61], v[2:3], v[76:77] op_sel_hi:[0,1,1]
	v_add_f32_e32 v0, v2, v0
	v_add_f32_e32 v0, v3, v0
	v_pk_fma_f32 v[4:5], v[60:61], v[4:5], v[78:79] op_sel_hi:[0,1,1]
	v_pk_fma_f32 v[10:11], v[62:63], v[18:19], v[10:11] op_sel_hi:[0,1,1]
	v_add_f32_e32 v0, v4, v0
	v_pk_fma_f32 v[28:29], v[60:61], v[54:55], v[10:11] op_sel_hi:[0,1,1]
	v_pk_fma_f32 v[30:31], v[60:61], v[52:53], v[12:13] op_sel_hi:[0,1,1]
	ds_read_b128 v[10:13], v99 offset:1472
	ds_read_b128 v[14:17], v99 offset:1504
	v_add_f32_e32 v0, v5, v0
	v_pk_fma_f32 v[6:7], v[60:61], v[6:7], v[80:81] op_sel_hi:[0,1,1]
	v_add_f32_e32 v0, v6, v0
	v_add_f32_e32 v0, v7, v0
	v_pk_fma_f32 v[8:9], v[60:61], v[8:9], v[82:83] op_sel_hi:[0,1,1]
	v_add_f32_e32 v0, v8, v0
	v_add_f32_e32 v0, v9, v0
	s_waitcnt lgkmcnt(0)
	v_pk_fma_f32 v[10:11], v[60:61], v[10:11], v[86:87] op_sel_hi:[0,1,1]
	v_add_f32_e32 v0, v10, v0
	v_add_f32_e32 v0, v11, v0
	v_pk_fma_f32 v[12:13], v[60:61], v[12:13], v[90:91] op_sel_hi:[0,1,1]
	v_add_f32_e32 v0, v12, v0
	v_add_f32_e32 v0, v13, v0
	v_pk_fma_f32 v[14:15], v[60:61], v[14:15], v[24:25] op_sel_hi:[0,1,1]
	v_add_f32_e32 v0, v14, v0
	v_pk_fma_f32 v[16:17], v[60:61], v[16:17], v[32:33] op_sel_hi:[0,1,1]
	v_add_f32_e32 v0, v15, v0
	v_add_f32_e32 v0, v16, v0
	v_add_f32_e32 v0, v17, v0
	v_add_f32_e32 v0, v30, v0
	v_add_f32_e32 v0, v31, v0
	v_add_f32_e32 v0, v28, v0
	v_pk_fma_f32 v[22:23], v[60:61], v[56:57], v[22:23] op_sel_hi:[0,1,1]
	v_add_f32_e32 v0, v29, v0
	v_add_f32_e32 v0, v22, v0
	v_pk_fma_f32 v[26:27], v[60:61], v[58:59], v[26:27] op_sel_hi:[0,1,1]
	v_add_f32_e32 v0, v23, v0
	v_add_f32_e32 v0, v26, v0
	v_add_f32_e32 v0, v27, v0
	v_mov_b32_e32 v24, v0
	v_mov_b32_e32 v25, v0
	s_nop 1
	v_permlane32_swap_b32_e32 v24, v25
	v_cndmask_b32_e32 v24, v24, v25, vcc
	v_add_f32_e32 v0, v0, v24
	v_mul_f32_e32 v0, 0x3c800000, v0
	v_pk_add_f32 v[24:25], v[68:69], v[0:1] op_sel_hi:[1,0] neg_lo:[0,1] neg_hi:[0,1]
	v_pk_add_f32 v[38:39], v[66:67], v[0:1] op_sel_hi:[1,0] neg_lo:[0,1] neg_hi:[0,1]
	v_pk_mul_f32 v[32:33], v[24:25], v[24:25]
	v_pk_mul_f32 v[40:41], v[38:39], v[38:39]
	v_pk_add_f32 v[34:35], v[34:35], v[0:1] op_sel_hi:[1,0] neg_lo:[0,1] neg_hi:[0,1]
	v_pk_add_f32 v[36:37], v[36:37], v[0:1] op_sel_hi:[1,0] neg_lo:[0,1] neg_hi:[0,1]
	v_pk_add_f32 v[46:47], v[2:3], v[0:1] op_sel_hi:[1,0] neg_lo:[0,1] neg_hi:[0,1]
	v_pk_add_f32 v[48:49], v[4:5], v[0:1] op_sel_hi:[1,0] neg_lo:[0,1] neg_hi:[0,1]
	v_pk_add_f32 v[50:51], v[6:7], v[0:1] op_sel_hi:[1,0] neg_lo:[0,1] neg_hi:[0,1]
	v_pk_add_f32 v[52:53], v[8:9], v[0:1] op_sel_hi:[1,0] neg_lo:[0,1] neg_hi:[0,1]
	v_pk_add_f32 v[54:55], v[10:11], v[0:1] op_sel_hi:[1,0] neg_lo:[0,1] neg_hi:[0,1]
	v_pk_add_f32 v[56:57], v[12:13], v[0:1] op_sel_hi:[1,0] neg_lo:[0,1] neg_hi:[0,1]
	v_pk_add_f32 v[58:59], v[14:15], v[0:1] op_sel_hi:[1,0] neg_lo:[0,1] neg_hi:[0,1]
	v_pk_add_f32 v[60:61], v[16:17], v[0:1] op_sel_hi:[1,0] neg_lo:[0,1] neg_hi:[0,1]
	v_pk_add_f32 v[30:31], v[30:31], v[0:1] op_sel_hi:[1,0] neg_lo:[0,1] neg_hi:[0,1]
	v_pk_add_f32 v[28:29], v[28:29], v[0:1] op_sel_hi:[1,0] neg_lo:[0,1] neg_hi:[0,1]
	v_pk_add_f32 v[22:23], v[22:23], v[0:1] op_sel_hi:[1,0] neg_lo:[0,1] neg_hi:[0,1]
	v_pk_add_f32 v[26:27], v[26:27], v[0:1] op_sel_hi:[1,0] neg_lo:[0,1] neg_hi:[0,1]
	v_add_f32_e32 v0, v32, v33
	v_add_f32_e32 v0, v40, v0
	v_pk_mul_f32 v[42:43], v[34:35], v[34:35]
	v_add_f32_e32 v0, v41, v0
	v_add_f32_e32 v0, v42, v0
	v_pk_mul_f32 v[44:45], v[36:37], v[36:37]
	v_add_f32_e32 v0, v43, v0
	v_add_f32_e32 v0, v44, v0
	v_pk_mul_f32 v[2:3], v[46:47], v[46:47]
	v_add_f32_e32 v0, v45, v0
	v_add_f32_e32 v0, v2, v0
	v_pk_mul_f32 v[4:5], v[48:49], v[48:49]
	v_add_f32_e32 v0, v3, v0
	v_add_f32_e32 v0, v4, v0
	v_pk_mul_f32 v[6:7], v[50:51], v[50:51]
	v_add_f32_e32 v0, v5, v0
	v_add_f32_e32 v0, v6, v0
	v_pk_mul_f32 v[8:9], v[52:53], v[52:53]
	v_add_f32_e32 v0, v7, v0
	v_add_f32_e32 v0, v8, v0
	v_pk_mul_f32 v[10:11], v[54:55], v[54:55]
	v_add_f32_e32 v0, v9, v0
	v_add_f32_e32 v0, v10, v0
	v_pk_mul_f32 v[12:13], v[56:57], v[56:57]
	v_add_f32_e32 v0, v11, v0
	v_add_f32_e32 v0, v12, v0
	v_pk_mul_f32 v[14:15], v[58:59], v[58:59]
	v_add_f32_e32 v0, v13, v0
	v_add_f32_e32 v0, v14, v0
	v_pk_mul_f32 v[16:17], v[60:61], v[60:61]
	v_add_f32_e32 v0, v15, v0
	v_add_f32_e32 v0, v16, v0
	v_pk_mul_f32 v[32:33], v[30:31], v[30:31]
	v_add_f32_e32 v0, v17, v0
	v_add_f32_e32 v0, v32, v0
	v_pk_mul_f32 v[2:3], v[28:29], v[28:29]
	v_add_f32_e32 v0, v33, v0
	v_add_f32_e32 v0, v2, v0
	v_pk_mul_f32 v[4:5], v[22:23], v[22:23]
	v_add_f32_e32 v0, v3, v0
	v_add_f32_e32 v0, v4, v0
	v_pk_mul_f32 v[6:7], v[26:27], v[26:27]
	v_add_f32_e32 v0, v5, v0
	v_add_f32_e32 v0, v6, v0
	v_add_f32_e32 v0, v7, v0
	v_mov_b32_e32 v2, v0
	v_mov_b32_e32 v3, v0
	s_nop 1
	v_permlane32_swap_b32_e32 v2, v3
	v_cndmask_b32_e32 v2, v2, v3, vcc
	v_add_f32_e32 v0, v0, v2
	v_mov_b32_e32 v2, 0x3727c5ac
	v_fmac_f32_e32 v2, 0x3c800000, v0
	ds_read_b128 v[18:21], v99 offset:3392
	v_rsq_f32_e32 v0, v2
	ds_read_b128 v[2:5], v99 offset:3136
	ds_read_b128 v[6:9], v99 offset:3168
	ds_read_b128 v[10:13], v99 offset:3424
	ds_read_b128 v[14:17], v99 offset:3456
	s_load_dwordx2 s[0:1], s[0:1], 0x40
	v_lshlrev_b32_e32 v101, 4, v1
	v_pk_mul_f32 v[24:25], v[24:25], v[0:1] op_sel_hi:[1,0]
	s_mov_b32 s2, 8
	s_waitcnt lgkmcnt(0)
	v_pk_fma_f32 v[86:87], v[2:3], v[24:25], v[18:19]
	v_pk_mul_f32 v[2:3], v[38:39], v[0:1] op_sel_hi:[1,0]
	v_pk_mul_f32 v[24:25], v[34:35], v[0:1] op_sel_hi:[1,0]
	v_pk_fma_f32 v[84:85], v[4:5], v[2:3], v[20:21]
	ds_read_b128 v[2:5], v99 offset:3200
	ds_read_b128 v[18:21], v99 offset:3232
	v_pk_fma_f32 v[82:83], v[6:7], v[24:25], v[10:11]
	v_pk_mul_f32 v[6:7], v[36:37], v[0:1] op_sel_hi:[1,0]
	v_pk_mul_f32 v[24:25], v[46:47], v[0:1] op_sel_hi:[1,0]
	v_pk_fma_f32 v[80:81], v[8:9], v[6:7], v[12:13]
	ds_read_b128 v[6:9], v99 offset:3488
	ds_read_b128 v[10:13], v99 offset:3520
	s_waitcnt lgkmcnt(0)
	v_pk_fma_f32 v[78:79], v[2:3], v[24:25], v[14:15]
	v_pk_mul_f32 v[2:3], v[48:49], v[0:1] op_sel_hi:[1,0]
	v_pk_mul_f32 v[24:25], v[50:51], v[0:1] op_sel_hi:[1,0]
	v_pk_fma_f32 v[76:77], v[4:5], v[2:3], v[16:17]
	ds_read_b128 v[2:5], v99 offset:3264
	ds_read_b128 v[14:17], v99 offset:3296
	v_pk_fma_f32 v[74:75], v[18:19], v[24:25], v[6:7]
	v_pk_mul_f32 v[6:7], v[52:53], v[0:1] op_sel_hi:[1,0]
	v_pk_mul_f32 v[24:25], v[54:55], v[0:1] op_sel_hi:[1,0]
	v_pk_fma_f32 v[72:73], v[20:21], v[6:7], v[8:9]
	ds_read_b128 v[6:9], v99 offset:3552
	ds_read_b128 v[18:21], v99 offset:3584
	s_waitcnt lgkmcnt(0)
	v_pk_fma_f32 v[70:71], v[2:3], v[24:25], v[10:11]
	v_pk_mul_f32 v[2:3], v[56:57], v[0:1] op_sel_hi:[1,0]
	v_pk_mul_f32 v[24:25], v[58:59], v[0:1] op_sel_hi:[1,0]
	v_pk_fma_f32 v[68:69], v[4:5], v[2:3], v[12:13]
	ds_read_b128 v[2:5], v99 offset:3328
	ds_read_b128 v[10:13], v99 offset:3360
	v_pk_fma_f32 v[66:67], v[14:15], v[24:25], v[6:7]
	v_pk_mul_f32 v[6:7], v[60:61], v[0:1] op_sel_hi:[1,0]
	v_pk_mul_f32 v[14:15], v[30:31], v[0:1] op_sel_hi:[1,0]
	v_pk_fma_f32 v[96:97], v[16:17], v[6:7], v[8:9]
	ds_read_b128 v[6:9], v99 offset:3616
	s_waitcnt lgkmcnt(0)
	v_pk_fma_f32 v[88:89], v[2:3], v[14:15], v[18:19]
	v_pk_mul_f32 v[2:3], v[28:29], v[0:1] op_sel_hi:[1,0]
	s_waitcnt vmcnt(0)
	v_cvt_pkrtz_f16_f32 v48, v86, v87
	v_pk_fma_f32 v[90:91], v[4:5], v[2:3], v[20:21]
	v_pk_mul_f32 v[2:3], v[22:23], v[0:1] op_sel_hi:[1,0]
	v_cvt_pkrtz_f16_f32 v49, v84, v85
	v_pk_fma_f32 v[92:93], v[10:11], v[2:3], v[6:7]
	v_pk_mul_f32 v[2:3], v[26:27], v[0:1] op_sel_hi:[1,0]
	v_mov_b32_e32 v0, 0
	v_pk_fma_f32 v[94:95], v[12:13], v[2:3], v[8:9]
	v_cvt_pkrtz_f16_f32 v50, v82, v83
	v_cvt_pkrtz_f16_f32 v51, v80, v81
	v_cvt_pkrtz_f16_f32 v52, v78, v79
	v_cvt_pkrtz_f16_f32 v53, v76, v77
	v_cvt_pkrtz_f16_f32 v54, v74, v75
	v_cvt_pkrtz_f16_f32 v55, v72, v73
	v_cvt_pkrtz_f16_f32 v56, v70, v71
	v_cvt_pkrtz_f16_f32 v57, v68, v69
	v_cvt_pkrtz_f16_f32 v58, v66, v67
	v_cvt_pkrtz_f16_f32 v59, v96, v97
	v_cvt_pkrtz_f16_f32 v60, v88, v89
	v_cvt_pkrtz_f16_f32 v61, v90, v91
	v_cvt_pkrtz_f16_f32 v62, v92, v93
	v_cvt_pkrtz_f16_f32 v63, v94, v95
	v_mov_b32_e32 v1, v0
	v_mov_b32_e32 v2, v0
	v_mov_b32_e32 v3, v0
	v_mov_b32_e32 v4, v0
	v_mov_b32_e32 v5, v0
	v_mov_b32_e32 v6, v0
	v_mov_b32_e32 v7, v0
	v_mov_b32_e32 v8, v0
	v_mov_b32_e32 v9, v0
	v_mov_b32_e32 v10, v0
	v_mov_b32_e32 v11, v0
	v_mov_b32_e32 v12, v0
	v_mov_b32_e32 v13, v0
	v_mov_b32_e32 v14, v0
	v_mov_b32_e32 v15, v0
	v_mov_b32_e32 v16, v0
	v_mov_b32_e32 v17, v0
	v_mov_b32_e32 v18, v0
	v_mov_b32_e32 v19, v0
	v_mov_b32_e32 v20, v0
	v_mov_b32_e32 v21, v0
	v_mov_b32_e32 v22, v0
	v_mov_b32_e32 v23, v0
	v_mov_b32_e32 v24, v0
	v_mov_b32_e32 v25, v0
	v_mov_b32_e32 v26, v0
	v_mov_b32_e32 v27, v0
	v_mov_b32_e32 v28, v0
	v_mov_b32_e32 v29, v0
	v_mov_b32_e32 v30, v0
	v_mov_b32_e32 v31, v0
	v_or_b32_e32 v102, 0x8000, v101
	s_waitcnt vmcnt(0)
	s_barrier
	v_add_u32_e32 v156, 0x10740, v98
	s_mov_b32 s2, 8
.Lmy_ffn3_k1:
	ds_read_b128 v[32:35], v156
	ds_read_b128 v[36:39], v156 offset:32
	ds_read_b128 v[40:43], v156 offset:64
	ds_read_b128 v[44:47], v156 offset:96
	ds_read_b128 v[140:143], v101
	ds_read_b128 v[144:147], v101 offset:1024
	ds_read_b128 v[148:151], v101 offset:2048
	ds_read_b128 v[152:155], v101 offset:3072
	v_add_u32_e32 v101, 0x1000, v101
	v_add_u32_e32 v156, 0x80, v156
	s_add_i32 s2, s2, -1
	s_waitcnt lgkmcnt(3)
	v_mfma_f32_32x32x16_f16 v[32:47], v[140:143], v[48:51], v[32:47]
	s_waitcnt lgkmcnt(2)
	v_mfma_f32_32x32x16_f16 v[32:47], v[144:147], v[52:55], v[32:47]
	s_waitcnt lgkmcnt(1)
	v_mfma_f32_32x32x16_f16 v[32:47], v[148:151], v[56:59], v[32:47]
	s_waitcnt lgkmcnt(0)
	v_mfma_f32_32x32x16_f16 v[32:47], v[152:155], v[60:63], v[32:47]
	ds_read_b128 v[112:115], v102
	ds_read_b128 v[116:119], v102 offset:16384
	ds_read_b128 v[104:107], v102 offset:1024
	ds_read_b128 v[120:123], v102 offset:17408
	v_add_u32_e32 v102, 0x800, v102
	s_cmp_lg_u32 s2, 0
	s_nop 5
	v_max_f32_e32 v32, 0, v32
	v_max_f32_e32 v33, 0, v33
	v_max_f32_e32 v34, 0, v34
	v_max_f32_e32 v35, 0, v35
	v_max_f32_e32 v36, 0, v36
	v_max_f32_e32 v37, 0, v37
	v_max_f32_e32 v38, 0, v38
	v_max_f32_e32 v39, 0, v39
	v_cvt_pkrtz_f16_f32 v32, v32, v33
	v_cvt_pkrtz_f16_f32 v33, v34, v35
	v_cvt_pkrtz_f16_f32 v34, v36, v37
	v_cvt_pkrtz_f16_f32 v35, v38, v39
	s_waitcnt lgkmcnt(2)
	s_nop 0
	v_mfma_f32_32x32x16_f16 v[16:31], v[112:115], v[32:35], v[16:31]
	v_mfma_f32_32x32x16_f16 v[0:15], v[116:119], v[32:35], v[0:15]
	v_max_f32_e32 v40, 0, v40
	v_max_f32_e32 v41, 0, v41
	v_max_f32_e32 v42, 0, v42
	v_max_f32_e32 v43, 0, v43
	v_max_f32_e32 v44, 0, v44
	v_max_f32_e32 v45, 0, v45
	v_max_f32_e32 v46, 0, v46
	v_max_f32_e32 v47, 0, v47
	v_cvt_pkrtz_f16_f32 v32, v40, v41
	v_cvt_pkrtz_f16_f32 v33, v42, v43
	v_cvt_pkrtz_f16_f32 v34, v44, v45
	v_cvt_pkrtz_f16_f32 v35, v46, v47
	s_waitcnt lgkmcnt(0)
	s_nop 0
	v_mfma_f32_32x32x16_f16 v[16:31], v[104:107], v[32:35], v[16:31]
	v_mfma_f32_32x32x16_f16 v[0:15], v[120:123], v[32:35], v[0:15]
	s_cbranch_scc1 .Lmy_ffn3_k1
	ds_read_b128 v[48:51], v99 offset:2880
	ds_read_b128 v[52:55], v99 offset:2912
	ds_read_b128 v[56:59], v99 offset:3008
	ds_read_b128 v[60:63], v99 offset:3040
	ds_read_b128 v[102:105], v99 offset:2944
	ds_read_b128 v[106:109], v99 offset:2976
	ds_read_b128 v[110:113], v99 offset:3072
	ds_read_b128 v[114:117], v99 offset:3104
	s_waitcnt lgkmcnt(7)
	s_nop 0
	v_pk_add_f32 v[16:17], v[16:17], v[48:49]
	v_pk_add_f32 v[18:19], v[18:19], v[50:51]
	v_pk_add_f32 v[16:17], v[86:87], v[16:17]
	v_pk_add_f32 v[18:19], v[84:85], v[18:19]
	v_add_f32_e32 v48, 0, v16
	v_add_f32_e32 v48, v17, v48
	v_add_f32_e32 v48, v18, v48
	s_waitcnt lgkmcnt(6)
	v_pk_add_f32 v[20:21], v[20:21], v[52:53]
	v_add_f32_e32 v48, v19, v48
	v_pk_add_f32 v[20:21], v[82:83], v[20:21]
	v_pk_add_f32 v[22:23], v[22:23], v[54:55]
	v_add_f32_e32 v48, v20, v48
	v_add_f32_e32 v48, v21, v48
	v_pk_add_f32 v[22:23], v[80:81], v[22:23]
	s_waitcnt lgkmcnt(3)
	v_pk_add_f32 v[24:25], v[24:25], v[102:103]
	v_add_f32_e32 v48, v22, v48
	v_add_f32_e32 v48, v23, v48
	v_pk_add_f32 v[24:25], v[78:79], v[24:25]
	v_pk_add_f32 v[26:27], v[26:27], v[104:105]
	v_add_f32_e32 v48, v24, v48
	v_add_f32_e32 v48, v25, v48
	v_pk_add_f32 v[26:27], v[76:77], v[26:27]
	s_waitcnt lgkmcnt(2)
	v_pk_add_f32 v[28:29], v[28:29], v[106:107]
	v_add_f32_e32 v48, v26, v48
	v_add_f32_e32 v48, v27, v48
	v_pk_add_f32 v[28:29], v[74:75], v[28:29]
	v_pk_add_f32 v[30:31], v[30:31], v[108:109]
	v_add_f32_e32 v48, v28, v48
	v_add_f32_e32 v48, v29, v48
	v_pk_add_f32 v[30:31], v[72:73], v[30:31]
	v_pk_add_f32 v[0:1], v[0:1], v[56:57]
	v_add_f32_e32 v48, v30, v48
	v_add_f32_e32 v48, v31, v48
	v_pk_add_f32 v[0:1], v[70:71], v[0:1]
	v_pk_add_f32 v[2:3], v[2:3], v[58:59]
	v_add_f32_e32 v48, v0, v48
	v_add_f32_e32 v48, v1, v48
	v_pk_add_f32 v[2:3], v[68:69], v[2:3]
	v_pk_add_f32 v[4:5], v[4:5], v[60:61]
	v_add_f32_e32 v48, v2, v48
	v_add_f32_e32 v48, v3, v48
	v_pk_add_f32 v[4:5], v[66:67], v[4:5]
	v_pk_add_f32 v[6:7], v[6:7], v[62:63]
	v_add_f32_e32 v48, v4, v48
	v_pk_add_f32 v[6:7], v[96:97], v[6:7]
	v_add_f32_e32 v48, v5, v48
	s_waitcnt lgkmcnt(1)
	v_pk_add_f32 v[8:9], v[8:9], v[110:111]
	v_add_f32_e32 v48, v6, v48
	v_pk_add_f32 v[8:9], v[88:89], v[8:9]
	v_add_f32_e32 v48, v7, v48
	v_pk_add_f32 v[10:11], v[10:11], v[112:113]
	v_add_f32_e32 v48, v8, v48
	v_pk_add_f32 v[10:11], v[90:91], v[10:11]
	v_add_f32_e32 v48, v9, v48
	s_waitcnt lgkmcnt(0)
	v_pk_add_f32 v[12:13], v[12:13], v[114:115]
	v_add_f32_e32 v48, v10, v48
	v_pk_add_f32 v[12:13], v[92:93], v[12:13]
	v_add_f32_e32 v48, v11, v48
	v_pk_add_f32 v[14:15], v[14:15], v[116:117]
	v_add_f32_e32 v48, v12, v48
	v_pk_add_f32 v[14:15], v[94:95], v[14:15]
	v_add_f32_e32 v48, v13, v48
	v_add_f32_e32 v48, v14, v48
	v_add_f32_e32 v48, v15, v48
	v_mov_b32_e32 v49, v48
	v_mov_b32_e32 v50, v48
	s_nop 1
	v_permlane32_swap_b32_e32 v49, v50
	v_cndmask_b32_e32 v49, v49, v50, vcc
	v_add_f32_e32 v48, v48, v49
	v_mul_f32_e32 v48, 0x3c800000, v48
	v_pk_add_f32 v[16:17], v[16:17], v[48:49] op_sel_hi:[1,0] neg_lo:[0,1] neg_hi:[0,1]
	v_pk_add_f32 v[18:19], v[18:19], v[48:49] op_sel_hi:[1,0] neg_lo:[0,1] neg_hi:[0,1]
	v_pk_mul_f32 v[50:51], v[16:17], v[16:17]
	v_pk_mul_f32 v[52:53], v[18:19], v[18:19]
	v_add_f32_e32 v50, v50, v51
	v_pk_add_f32 v[20:21], v[20:21], v[48:49] op_sel_hi:[1,0] neg_lo:[0,1] neg_hi:[0,1]
	v_add_f32_e32 v50, v52, v50
	v_pk_mul_f32 v[54:55], v[20:21], v[20:21]
	v_add_f32_e32 v50, v53, v50
	v_pk_add_f32 v[22:23], v[22:23], v[48:49] op_sel_hi:[1,0] neg_lo:[0,1] neg_hi:[0,1]
	v_add_f32_e32 v50, v54, v50
	v_pk_mul_f32 v[56:57], v[22:23], v[22:23]
	v_add_f32_e32 v50, v55, v50
	v_pk_add_f32 v[24:25], v[24:25], v[48:49] op_sel_hi:[1,0] neg_lo:[0,1] neg_hi:[0,1]
	v_add_f32_e32 v50, v56, v50
	v_pk_mul_f32 v[58:59], v[24:25], v[24:25]
	v_add_f32_e32 v50, v57, v50
	v_pk_add_f32 v[26:27], v[26:27], v[48:49] op_sel_hi:[1,0] neg_lo:[0,1] neg_hi:[0,1]
	v_add_f32_e32 v50, v58, v50
	v_pk_mul_f32 v[60:61], v[26:27], v[26:27]
	v_add_f32_e32 v50, v59, v50
	v_pk_add_f32 v[28:29], v[28:29], v[48:49] op_sel_hi:[1,0] neg_lo:[0,1] neg_hi:[0,1]
	v_add_f32_e32 v50, v60, v50
	v_lshlrev_b64 v[62:63], 7, v[64:65]
	v_pk_mul_f32 v[64:65], v[28:29], v[28:29]
	v_add_f32_e32 v50, v61, v50
	v_pk_add_f32 v[30:31], v[30:31], v[48:49] op_sel_hi:[1,0] neg_lo:[0,1] neg_hi:[0,1]
	v_add_f32_e32 v50, v64, v50
	v_pk_mul_f32 v[66:67], v[30:31], v[30:31]
	v_add_f32_e32 v50, v65, v50
	v_pk_add_f32 v[0:1], v[0:1], v[48:49] op_sel_hi:[1,0] neg_lo:[0,1] neg_hi:[0,1]
	v_add_f32_e32 v50, v66, v50
	v_pk_mul_f32 v[68:69], v[0:1], v[0:1]
	v_add_f32_e32 v50, v67, v50
	v_pk_add_f32 v[2:3], v[2:3], v[48:49] op_sel_hi:[1,0] neg_lo:[0,1] neg_hi:[0,1]
	v_add_f32_e32 v50, v68, v50
	v_pk_mul_f32 v[70:71], v[2:3], v[2:3]
	v_add_f32_e32 v50, v69, v50
	v_pk_add_f32 v[4:5], v[4:5], v[48:49] op_sel_hi:[1,0] neg_lo:[0,1] neg_hi:[0,1]
	v_add_f32_e32 v50, v70, v50
	v_pk_mul_f32 v[72:73], v[4:5], v[4:5]
	v_add_f32_e32 v50, v71, v50
	v_pk_add_f32 v[6:7], v[6:7], v[48:49] op_sel_hi:[1,0] neg_lo:[0,1] neg_hi:[0,1]
	v_add_f32_e32 v50, v72, v50
	v_pk_add_f32 v[8:9], v[8:9], v[48:49] op_sel_hi:[1,0] neg_lo:[0,1] neg_hi:[0,1]
	v_pk_add_f32 v[10:11], v[10:11], v[48:49] op_sel_hi:[1,0] neg_lo:[0,1] neg_hi:[0,1]
	v_pk_add_f32 v[12:13], v[12:13], v[48:49] op_sel_hi:[1,0] neg_lo:[0,1] neg_hi:[0,1]
	v_pk_add_f32 v[14:15], v[14:15], v[48:49] op_sel_hi:[1,0] neg_lo:[0,1] neg_hi:[0,1]
	v_pk_mul_f32 v[48:49], v[6:7], v[6:7]
	v_add_f32_e32 v50, v73, v50
	v_add_f32_e32 v48, v48, v50
	v_pk_mul_f32 v[74:75], v[8:9], v[8:9]
	v_add_f32_e32 v48, v49, v48
	v_add_f32_e32 v48, v74, v48
	v_pk_mul_f32 v[76:77], v[10:11], v[10:11]
	v_add_f32_e32 v48, v75, v48
	v_add_f32_e32 v48, v76, v48
	v_pk_mul_f32 v[78:79], v[12:13], v[12:13]
	v_add_f32_e32 v48, v77, v48
	v_add_f32_e32 v48, v78, v48
	v_pk_mul_f32 v[80:81], v[14:15], v[14:15]
	v_add_f32_e32 v48, v79, v48
	v_add_f32_e32 v48, v80, v48
	v_add_f32_e32 v48, v81, v48
	v_mov_b32_e32 v49, v48
	v_mov_b32_e32 v50, v48
	s_nop 1
	v_permlane32_swap_b32_e32 v49, v50
	v_cndmask_b32_e32 v49, v49, v50, vcc
	v_add_f32_e32 v48, v48, v49
	v_mov_b32_e32 v49, 0x3727c5ac
	v_fmac_f32_e32 v49, 0x3c800000, v48
	v_rsq_f32_e32 v48, v49
	ds_read_b128 v[118:121], v99 offset:3648
	ds_read_b128 v[122:125], v99 offset:3680
	ds_read_b128 v[126:129], v99 offset:3904
	ds_read_b128 v[130:133], v99 offset:3936
	ds_read_b128 v[134:137], v99 offset:3712
	ds_read_b128 v[138:141], v99 offset:3744
	ds_read_b128 v[142:145], v99 offset:3968
	ds_read_b128 v[146:149], v99 offset:4000
	ds_read_b128 v[150:153], v99 offset:3776
	ds_read_b128 v[154:157], v99 offset:3808
	ds_read_b128 v[158:161], v99 offset:4032
	ds_read_b128 v[162:165], v99 offset:4064
	ds_read_b128 v[40:43], v99 offset:3840
	ds_read_b128 v[32:35], v99 offset:3872
	ds_read_b128 v[44:47], v99 offset:4096
	ds_read_b128 v[36:39], v99 offset:4128
	v_lshl_add_u64 v[62:63], s[0:1], 0, v[62:63]
	v_lshlrev_b32_e32 v50, 1, v100
	v_pk_mul_f32 v[0:1], v[0:1], v[48:49] op_sel_hi:[1,0]
	v_pk_mul_f32 v[2:3], v[2:3], v[48:49] op_sel_hi:[1,0]
	v_mov_b32_e32 v51, 0
	s_waitcnt lgkmcnt(5)
	v_pk_fma_f32 v[0:1], v[150:151], v[0:1], v[158:159]
	v_pk_fma_f32 v[2:3], v[152:153], v[2:3], v[160:161]
	v_pk_mul_f32 v[4:5], v[4:5], v[48:49] op_sel_hi:[1,0]
	v_pk_mul_f32 v[6:7], v[6:7], v[48:49] op_sel_hi:[1,0]
	v_lshl_add_u64 v[50:51], v[62:63], 0, v[50:51]
	s_waitcnt lgkmcnt(4)
	v_pk_fma_f32 v[4:5], v[154:155], v[4:5], v[162:163]
	v_pk_fma_f32 v[6:7], v[156:157], v[6:7], v[164:165]
	v_cvt_pk_f16_f32 v0, v0, v1
	v_cvt_pk_f16_f32 v1, v2, v3
	global_store_dwordx2 v[50:51], v[0:1], off offset:64
	v_cvt_pk_f16_f32 v0, v4, v5
	v_cvt_pk_f16_f32 v1, v6, v7
	v_pk_mul_f32 v[16:17], v[16:17], v[48:49] op_sel_hi:[1,0]
	v_pk_mul_f32 v[18:19], v[18:19], v[48:49] op_sel_hi:[1,0]
	global_store_dwordx2 v[50:51], v[0:1], off offset:80
	v_pk_mul_f32 v[0:1], v[8:9], v[48:49] op_sel_hi:[1,0]
	v_pk_mul_f32 v[2:3], v[10:11], v[48:49] op_sel_hi:[1,0]
	v_pk_fma_f32 v[16:17], v[118:119], v[16:17], v[126:127]
	v_pk_fma_f32 v[18:19], v[120:121], v[18:19], v[128:129]
	v_pk_mul_f32 v[20:21], v[20:21], v[48:49] op_sel_hi:[1,0]
	v_pk_mul_f32 v[22:23], v[22:23], v[48:49] op_sel_hi:[1,0]
	s_waitcnt lgkmcnt(1)
	v_pk_fma_f32 v[0:1], v[40:41], v[0:1], v[44:45]
	v_pk_fma_f32 v[2:3], v[42:43], v[2:3], v[46:47]
	v_pk_fma_f32 v[20:21], v[122:123], v[20:21], v[130:131]
	v_pk_fma_f32 v[22:23], v[124:125], v[22:23], v[132:133]
	v_pk_mul_f32 v[24:25], v[24:25], v[48:49] op_sel_hi:[1,0]
	v_pk_mul_f32 v[26:27], v[26:27], v[48:49] op_sel_hi:[1,0]
	v_cvt_pk_f16_f32 v16, v16, v17
	v_cvt_pk_f16_f32 v17, v18, v19
	v_cvt_pk_f16_f32 v0, v0, v1
	v_cvt_pk_f16_f32 v1, v2, v3
	v_pk_fma_f32 v[24:25], v[134:135], v[24:25], v[142:143]
	v_pk_fma_f32 v[26:27], v[136:137], v[26:27], v[144:145]
	v_pk_mul_f32 v[28:29], v[28:29], v[48:49] op_sel_hi:[1,0]
	v_pk_mul_f32 v[30:31], v[30:31], v[48:49] op_sel_hi:[1,0]
	global_store_dwordx2 v[50:51], v[16:17], off
	v_cvt_pk_f16_f32 v16, v20, v21
	v_cvt_pk_f16_f32 v17, v22, v23
	global_store_dwordx2 v[50:51], v[0:1], off offset:96
	v_pk_mul_f32 v[0:1], v[12:13], v[48:49] op_sel_hi:[1,0]
	v_pk_mul_f32 v[2:3], v[14:15], v[48:49] op_sel_hi:[1,0]
	v_pk_fma_f32 v[28:29], v[138:139], v[28:29], v[146:147]
	v_pk_fma_f32 v[30:31], v[140:141], v[30:31], v[148:149]
	global_store_dwordx2 v[50:51], v[16:17], off offset:16
	v_cvt_pk_f16_f32 v16, v24, v25
	v_cvt_pk_f16_f32 v17, v26, v27
	s_waitcnt lgkmcnt(0)
	v_pk_fma_f32 v[0:1], v[32:33], v[0:1], v[36:37]
	v_pk_fma_f32 v[2:3], v[34:35], v[2:3], v[38:39]
	global_store_dwordx2 v[50:51], v[16:17], off offset:32
	v_cvt_pk_f16_f32 v16, v28, v29
	v_cvt_pk_f16_f32 v17, v30, v31
	v_cvt_pk_f16_f32 v0, v0, v1
	v_cvt_pk_f16_f32 v1, v2, v3
	global_store_dwordx2 v[50:51], v[16:17], off offset:48
	global_store_dwordx2 v[50:51], v[0:1], off offset:112
	s_endpgm
